# baseline (speedup 1.0000x reference)
.LBB0_30:
	v_mov_b32_e32 v209, v245
	v_mul_u32_u24_e32 v100, 0x4400, v213
	v_add_u32_e32 v100, v100, v210
	v_mul_u32_u24_e32 v101, 0x4540, v213
	v_add_u32_e32 v101, v101, v210
	v_mov_b32_e32 v253, v210
	v_add_u32_e32 v254, 0xcfc0, v210
	v_add_u32_e32 v255, 0x19f80, v210
	global_load_dwordx4 v[104:107], v100, s[36:37]
	global_load_dwordx4 v[108:111], v100, s[36:37] offset:1024
	global_load_dwordx4 v[112:115], v100, s[36:37] offset:2048
	global_load_dwordx4 v[116:119], v100, s[36:37] offset:3072
	v_add_u32_e32 v102, 0x1000, v100
	global_load_dwordx4 v[120:123], v102, s[36:37]
	global_load_dwordx4 v[124:127], v102, s[36:37] offset:1024
	global_load_dwordx4 v[128:131], v102, s[36:37] offset:2048
	global_load_dwordx4 v[132:135], v102, s[36:37] offset:3072
	v_add_u32_e32 v102, 0x2000, v100
	global_load_dwordx4 v[136:139], v102, s[36:37]
	global_load_dwordx4 v[140:143], v102, s[36:37] offset:1024
	global_load_dwordx4 v[144:147], v102, s[36:37] offset:2048
	global_load_dwordx4 v[148:151], v102, s[36:37] offset:3072
	v_add_u32_e32 v102, 0x3000, v100
	global_load_dwordx4 v[152:155], v102, s[36:37]
	global_load_dwordx4 v[156:159], v102, s[36:37] offset:1024
	global_load_dwordx4 v[160:163], v102, s[36:37] offset:2048
	global_load_dwordx4 v[164:167], v102, s[36:37] offset:3072
	v_add_u32_e32 v102, 0x4000, v100
	global_load_dwordx4 v[168:171], v102, s[36:37]
	s_waitcnt vmcnt(0)
	ds_write_b128 v101, v[104:107]
	ds_write_b128 v101, v[108:111] offset:1024
	ds_write_b128 v101, v[112:115] offset:2048
	ds_write_b128 v101, v[116:119] offset:3072
	ds_write_b128 v101, v[120:123] offset:4096
	ds_write_b128 v101, v[124:127] offset:5120
	ds_write_b128 v101, v[128:131] offset:6144
	ds_write_b128 v101, v[132:135] offset:7168
	ds_write_b128 v101, v[136:139] offset:8192
	ds_write_b128 v101, v[140:143] offset:9216
	ds_write_b128 v101, v[144:147] offset:10240
	ds_write_b128 v101, v[148:151] offset:11264
	ds_write_b128 v101, v[152:155] offset:12288
	ds_write_b128 v101, v[156:159] offset:13312
	ds_write_b128 v101, v[160:163] offset:14336
	ds_write_b128 v101, v[164:167] offset:15360
	ds_write_b128 v101, v[168:171] offset:16384
	v_readfirstlane_b32 s0, v213
	s_cmp_lt_i32 s0, 3
	s_waitcnt lgkmcnt(0)
	s_barrier
	s_cbranch_scc0 .LBB0_33
	v_mov_b32_e32 v83, 0
	v_mov_b32_e32 v211, v83
	v_lshl_add_u64 v[156:157], s[36:37], 0, v[210:211]
	s_movk_i32 s0, 0x3000
	v_add_co_u32_e32 v68, vcc, s0, v156
	s_movk_i32 s0, 0x2000
	s_nop 0
	v_addc_co_u32_e32 v69, vcc, 0, v157, vcc
	ds_read_b128 v[0:3], v253 offset:8192
	v_add_co_u32_e32 v70, vcc, s0, v156
	s_movk_i32 s0, 0x1000
	s_nop 0
	v_addc_co_u32_e32 v71, vcc, 0, v157, vcc
	ds_read_b128 v[16:19], v253 offset:9216
	ds_read_b128 v[56:59], v253
	ds_read_b128 v[52:55], v253 offset:1024
	ds_read_b128 v[48:51], v253 offset:2048
	ds_read_b128 v[44:47], v253 offset:3072
	v_add_co_u32_e32 v20, vcc, s0, v156
	s_movk_i32 s0, 0x50
	s_nop 0
	v_addc_co_u32_e32 v21, vcc, 0, v157, vcc
	ds_read_b128 v[40:43], v253 offset:4096
	ds_read_b128 v[36:39], v253 offset:5120
	ds_read_b128 v[32:35], v253 offset:6144
	ds_read_b128 v[60:63], v253 offset:12288
	ds_read_b128 v[72:75], v253 offset:7168
	ds_read_b128 v[76:79], v253 offset:10240
	v_lshl_or_b32 v20, v213, 5, v212
	v_mov_b32_e32 v21, 0x4f
	v_cmp_gt_u32_e64 s[0:1], s0, v20
	s_lshl_b32 s2, s2, 2
	s_movk_i32 s3, 0x4000
	v_cndmask_b32_e64 v100, v21, v20, s[0:1]
	v_lshl_or_b32 v64, v100, 7, v208
	v_add_u32_e32 v127, 0x22a00, v64
	ds_read_b128 v[64:67], v127
	ds_read_b128 v[84:87], v127 offset:32
	s_mov_b32 s9, 0x66666667
	v_add_co_u32_e32 v108, vcc, s3, v156
	s_movk_i32 s10, 0x5000
	s_nop 0
	v_addc_co_u32_e32 v109, vcc, 0, v157, vcc
	v_add_co_u32_e32 v152, vcc, s10, v156
	v_lshlrev_b32_e32 v82, 1, v214
	s_nop 0
	v_addc_co_u32_e32 v153, vcc, 0, v157, vcc
	v_mov_b32_e32 v126, 0x3727c5ac
	s_mov_b32 s8, 0xf800000
	v_mov_b32_e32 v208, 0x260
	v_mov_b32_e32 v80, s26
	v_mov_b32_e32 v81, s27
	s_and_b64 s[0:1], s[4:5], s[0:1]
	s_waitcnt lgkmcnt(12)
	v_mfma_f32_32x32x16_f16 v[16:31], v[16:19], v[96:99], 0
	v_mfma_f32_32x32x16_f16 v[0:15], v[0:3], v[96:99], 0
	s_waitcnt lgkmcnt(1)
	v_mfma_f32_32x32x16_f16 v[0:15], v[56:59], v[64:67], v[0:15]
	s_waitcnt lgkmcnt(1)
	v_mfma_f32_32x32x16_f16 v[16:31], v[52:55], v[64:67], v[16:31]
	v_mul_lo_u16_e32 v52, 0xcd, v100
	v_lshrrev_b16_e32 v52, 10, v52
	v_lshlrev_b32_e32 v102, 10, v52
	v_lshrrev_b32_e32 v101, 2, v52
	v_sub_u32_e32 v103, s2, v52
	s_waitcnt lgkmcnt(0)
	v_mfma_f32_32x32x16_f16 v[0:15], v[48:51], v[84:87], v[0:15]
	ds_read_b128 v[48:51], v127 offset:64
	ds_read_b128 v[88:91], v127 offset:96
	s_waitcnt lgkmcnt(2)
	v_mfma_f32_32x32x16_f16 v[16:31], v[44:47], v[84:87], v[16:31]
	ds_read_b128 v[84:87], v253 offset:18752
	ds_read_b128 v[92:95], v253 offset:19776
	ds_read_b128 v[120:123], v253 offset:11264
	ds_read_b128 v[52:55], v253 offset:13312
	ds_read_b128 v[56:59], v253 offset:14336
	ds_read_b128 v[44:47], v253 offset:15360
	ds_read_b128 v[64:67], v253 offset:16384
	s_waitcnt lgkmcnt(8)
	v_mfma_f32_32x32x16_f16 v[0:15], v[40:43], v[48:51], v[0:15]
	v_and_b32_e32 v40, 0xc00, v102
	v_add3_u32 v40, v103, v101, v40
	v_mad_u64_u32 v[158:159], s[2:3], v40, 5, v[100:101]
	v_mul_hi_i32 v42, v158, s9
	v_lshlrev_b32_e32 v40, 6, v158
	v_ashrrev_i32_e32 v41, 31, v40
	s_waitcnt lgkmcnt(8)
	v_mfma_f32_32x32x16_f16 v[16:31], v[36:39], v[48:51], v[16:31]
	v_lshrrev_b32_e32 v38, 31, v42
	v_ashrrev_i32_e32 v39, 1, v42
	v_add_u32_e32 v159, v39, v38
	v_lshlrev_b32_e32 v68, 6, v159
	v_ashrrev_i32_e32 v69, 31, v68
	v_lshl_add_u64 v[48:49], v[68:69], 2, s[24:25]
	v_lshl_add_u64 v[36:37], v[40:41], 1, s[6:7]
	s_waitcnt lgkmcnt(7)
	v_mfma_f32_32x32x16_f16 v[0:15], v[32:35], v[88:91], v[0:15]
	v_lshl_add_u64 v[70:71], v[36:37], 0, v[82:83]
	v_lshlrev_b32_e32 v82, 2, v216
	v_lshl_add_u64 v[116:117], v[48:49], 0, v[82:83]
	global_load_dwordx4 v[32:35], v82, s[28:29]
	global_load_dwordx4 v[36:39], v82, s[28:29] offset:32
	global_load_dwordx4 v[40:43], v82, s[28:29] offset:64
	global_load_dwordx4 v[128:131], v82, s[28:29] offset:96
	v_add_u32_e32 v68, 0x40000, v68
	s_mov_b32 s6, 0xd000
	s_mov_b32 s7, 0xc000
	s_waitcnt lgkmcnt(7)
	v_mfma_f32_32x32x16_f16 v[16:31], v[72:75], v[88:91], v[16:31]
	s_nop 11
	v_add_f32_e32 v69, v0, v16
	v_add_f32_e32 v90, v1, v17
	v_add_f32_e32 v69, 0, v69
	v_add_f32_e32 v91, v2, v18
	v_add_f32_e32 v69, v90, v69
	v_add_f32_e32 v100, v3, v19
	v_add_f32_e32 v69, v91, v69
	v_add_f32_e32 v101, v4, v20
	v_add_f32_e32 v69, v100, v69
	v_add_f32_e32 v102, v5, v21
	v_add_f32_e32 v69, v101, v69
	v_pk_add_f32 v[48:49], v[6:7], v[22:23]
	v_add_f32_e32 v69, v102, v69
	v_add_f32_e32 v48, v48, v69
	v_pk_add_f32 v[50:51], v[8:9], v[24:25]
	v_add_f32_e32 v48, v49, v48
	v_add_f32_e32 v48, v50, v48
	v_pk_add_f32 v[72:73], v[10:11], v[26:27]
	v_add_f32_e32 v48, v51, v48
	v_add_f32_e32 v48, v72, v48
	v_pk_add_f32 v[74:75], v[12:13], v[28:29]
	v_add_f32_e32 v48, v73, v48
	v_add_f32_e32 v48, v74, v48
	v_pk_add_f32 v[88:89], v[14:15], v[30:31]
	v_add_f32_e32 v48, v75, v48
	v_add_f32_e32 v48, v88, v48
	v_add_f32_e32 v69, v89, v48
	ds_bpermute_b32 v72, v209, v69
	global_load_dwordx4 v[48:51], v[116:117], off
	global_load_dwordx4 v[88:91], v[116:117], off offset:32
	global_load_dwordx4 v[132:135], v[116:117], off offset:64
	global_load_dwordx4 v[136:139], v[116:117], off offset:96
	global_load_dwordx4 v[104:107], v[70:71], off
	global_load_dwordx4 v[100:103], v[70:71], off offset:32
	global_load_dwordx4 v[140:143], v82, s[28:29] offset:128
	global_load_dwordx4 v[144:147], v82, s[28:29] offset:160
	global_load_dwordx4 v[148:151], v[116:117], off offset:128
	global_load_dwordx4 v[160:163], v82, s[28:29] offset:192
	global_load_dwordx4 v[164:167], v[116:117], off offset:160
	global_load_dwordx4 v[168:171], v[116:117], off offset:192
	ds_read_b128 v[172:175], v253 offset:17728
	s_waitcnt lgkmcnt(1)
	v_add_f32_e32 v69, v69, v72
	v_mul_f32_e32 v72, 0x3c800000, v69
	v_pk_add_f32 v[124:125], v[30:31], v[72:73] op_sel_hi:[1,0] neg_lo:[0,1] neg_hi:[0,1]
	v_pk_add_f32 v[154:155], v[14:15], v[72:73] op_sel_hi:[1,0] neg_lo:[0,1] neg_hi:[0,1]
	v_pk_add_f32 v[184:185], v[28:29], v[72:73] op_sel_hi:[1,0] neg_lo:[0,1] neg_hi:[0,1]
	v_pk_add_f32 v[186:187], v[12:13], v[72:73] op_sel_hi:[1,0] neg_lo:[0,1] neg_hi:[0,1]
	v_pk_add_f32 v[188:189], v[26:27], v[72:73] op_sel_hi:[1,0] neg_lo:[0,1] neg_hi:[0,1]
	v_pk_add_f32 v[190:191], v[10:11], v[72:73] op_sel_hi:[1,0] neg_lo:[0,1] neg_hi:[0,1]
	v_pk_add_f32 v[192:193], v[24:25], v[72:73] op_sel_hi:[1,0] neg_lo:[0,1] neg_hi:[0,1]
	v_pk_add_f32 v[194:195], v[8:9], v[72:73] op_sel_hi:[1,0] neg_lo:[0,1] neg_hi:[0,1]
	v_pk_add_f32 v[196:197], v[22:23], v[72:73] op_sel_hi:[1,0] neg_lo:[0,1] neg_hi:[0,1]
	v_pk_add_f32 v[74:75], v[6:7], v[72:73] op_sel_hi:[1,0] neg_lo:[0,1] neg_hi:[0,1]
	v_pk_add_f32 v[198:199], v[20:21], v[72:73] op_sel_hi:[1,0] neg_lo:[0,1] neg_hi:[0,1]
	v_pk_add_f32 v[118:119], v[4:5], v[72:73] op_sel_hi:[1,0] neg_lo:[0,1] neg_hi:[0,1]
	v_pk_add_f32 v[200:201], v[18:19], v[72:73] op_sel_hi:[1,0] neg_lo:[0,1] neg_hi:[0,1]
	v_pk_add_f32 v[202:203], v[2:3], v[72:73] op_sel_hi:[1,0] neg_lo:[0,1] neg_hi:[0,1]
	v_pk_add_f32 v[204:205], v[16:17], v[72:73] op_sel_hi:[1,0] neg_lo:[0,1] neg_hi:[0,1]
	v_pk_add_f32 v[72:73], v[0:1], v[72:73] op_sel_hi:[1,0] neg_lo:[0,1] neg_hi:[0,1]
	global_load_dwordx4 v[112:115], v[70:71], off offset:64
	global_load_dwordx4 v[108:111], v[70:71], off offset:96
	global_load_dwordx4 v[176:179], v82, s[28:29] offset:224
	global_load_dwordx4 v[180:183], v[116:117], off offset:224
	v_fma_f32 v0, v72, v72, 0
	v_fmac_f32_e32 v0, v204, v204
	v_fmac_f32_e32 v0, v73, v73
	v_fmac_f32_e32 v0, v205, v205
	v_fmac_f32_e32 v0, v202, v202
	v_fmac_f32_e32 v0, v200, v200
	v_fmac_f32_e32 v0, v203, v203
	v_fmac_f32_e32 v0, v201, v201
	v_fmac_f32_e32 v0, v118, v118
	v_fmac_f32_e32 v0, v198, v198
	v_fmac_f32_e32 v0, v119, v119
	v_fmac_f32_e32 v0, v199, v199
	v_fmac_f32_e32 v0, v74, v74
	v_fmac_f32_e32 v0, v196, v196
	v_fmac_f32_e32 v0, v75, v75
	v_fmac_f32_e32 v0, v197, v197
	v_fmac_f32_e32 v0, v194, v194
	v_fmac_f32_e32 v0, v192, v192
	v_fmac_f32_e32 v0, v195, v195
	v_fmac_f32_e32 v0, v193, v193
	v_fmac_f32_e32 v0, v190, v190
	v_fmac_f32_e32 v0, v188, v188
	v_fmac_f32_e32 v0, v191, v191
	v_fmac_f32_e32 v0, v189, v189
	v_fmac_f32_e32 v0, v186, v186
	v_fmac_f32_e32 v0, v184, v184
	v_fmac_f32_e32 v0, v187, v187
	v_fmac_f32_e32 v0, v185, v185
	v_fmac_f32_e32 v0, v154, v154
	v_fmac_f32_e32 v0, v124, v124
	v_fmac_f32_e32 v0, v155, v155
	v_fmac_f32_e32 v0, v125, v125
	ds_bpermute_b32 v1, v209, v0
	s_waitcnt lgkmcnt(0)
	v_add_f32_e32 v0, v0, v1
	v_fmamk_f32 v0, v0, 0x3c800000, v126
	v_mul_f32_e32 v1, 0x4f800000, v0
	v_cmp_gt_f32_e32 vcc, s8, v0
	s_nop 1
	v_cndmask_b32_e32 v0, v0, v1, vcc
	v_sqrt_f32_e32 v1, v0
	s_nop 0
	v_add_u32_e32 v2, -1, v1
	v_fma_f32 v3, -v2, v1, v0
	v_cmp_ge_f32_e64 s[2:3], 0, v3
	v_add_u32_e32 v3, 1, v1
	s_nop 0
	v_cndmask_b32_e64 v2, v1, v2, s[2:3]
	v_fma_f32 v1, -v3, v1, v0
	v_cmp_lt_f32_e64 s[2:3], 0, v1
	s_nop 1
	v_cndmask_b32_e64 v1, v2, v3, s[2:3]
	v_mul_f32_e32 v2, 0x37800000, v1
	v_cndmask_b32_e32 v1, v1, v2, vcc
	v_cmp_class_f32_e32 vcc, v0, v208
	s_nop 1
	v_cndmask_b32_e32 v69, v1, v0, vcc
	v_div_scale_f32 v16, s[2:3], v69, v69, 1.0
	v_rcp_f32_e32 v206, v16
	s_waitcnt lgkmcnt(0)
	v_mfma_f32_32x32x16_f16 v[0:15], v[84:87], v[96:99], 0
	ds_read_b128 v[84:87], v127 offset:10240
	s_mov_b32 s2, 0xa000
	v_fma_f32 v17, -v16, v206, 1.0
	v_fmac_f32_e32 v206, v17, v206
	v_div_scale_f32 v17, vcc, 1.0, v69, 1.0
	v_mul_f32_e32 v70, v17, v206
	v_fma_f32 v18, -v16, v70, v17
	v_fmac_f32_e32 v70, v18, v206
	v_fma_f32 v71, -v16, v70, v17
	s_waitcnt lgkmcnt(1)
	v_mfma_f32_32x32x16_f16 v[16:31], v[92:95], v[96:99], 0
	ds_read_b128 v[92:95], v127 offset:10272
	v_div_fmas_f32 v70, v71, v206, v70
	v_div_fixup_f32 v70, v70, v69, 1.0
	v_mul_f32_e64 v210, v118, v70
	v_mul_f32_e64 v211, v119, v70
	v_pk_mul_f32 v[206:207], v[74:75], v[70:71] op_sel_hi:[1,0]
	v_pk_mul_f32 v[74:75], v[202:203], v[70:71] op_sel_hi:[1,0]
	s_waitcnt vmcnt(14) lgkmcnt(2)
	v_pk_fma_f32 v[36:37], v[210:211], v[36:37], v[88:89]
	s_waitcnt vmcnt(14) lgkmcnt(1)
	v_mfma_f32_32x32x16_f16 v[0:15], v[76:79], v[84:87], v[0:15]
	v_fma_f32 v34, v74, v34, v50
	v_fma_f32 v35, v75, v35, v51
	v_fma_f32 v38, v206, v38, v90
	v_fma_f32 v39, v207, v39, v91
	v_cvt_pk_f16_f32 v50, v36, v37
	v_pk_mul_f32 v[36:37], v[154:155], v[70:71] op_sel_hi:[1,0]
	v_cvt_pk_f16_f32 v51, v38, v39
	v_pk_mul_f32 v[38:39], v[186:187], v[70:71] op_sel_hi:[1,0]
	s_waitcnt vmcnt(12) lgkmcnt(1)
	v_pk_fma_f32 v[36:37], v[36:37], v[130:131], v[138:139]
	v_mfma_f32_32x32x16_f16 v[16:31], v[120:123], v[84:87], v[16:31]
	ds_read_b128 v[84:87], v127 offset:10336
	v_mul_f32_e64 v72, v72, v70
	v_mul_f32_e64 v73, v73, v70
	v_mul_f32_e64 v88, v184, v70
	v_mul_f32_e64 v89, v185, v70
	v_pk_fma_f32 v[32:33], v[72:73], v[32:33], v[48:49]
	v_cvt_pk_f16_f32 v49, v34, v35
	v_cvt_pk_f16_f32 v48, v32, v33
	v_pk_mul_f32 v[32:33], v[190:191], v[70:71] op_sel_hi:[1,0]
	s_waitcnt vmcnt(12) lgkmcnt(1)
	v_mfma_f32_32x32x16_f16 v[0:15], v[60:63], v[92:95], v[0:15]
	v_fma_f32 v60, v38, v128, v136
	v_fma_f32 v61, v39, v129, v137
	v_mul_f32_e64 v62, v204, v70
	v_mul_f32_e64 v63, v205, v70
	v_mul_f32_e64 v34, v194, v70
	v_mul_f32_e64 v35, v195, v70
	s_waitcnt vmcnt(7) lgkmcnt(1)
	v_pk_fma_f32 v[62:63], v[62:63], v[140:141], v[148:149]
	v_pk_fma_f32 v[40:41], v[34:35], v[40:41], v[132:133]
	v_pk_fma_f32 v[42:43], v[32:33], v[42:43], v[134:135]
	global_load_dwordx4 v[116:119], v82, s[30:31]
	global_load_dwordx4 v[72:75], v82, s[30:31] offset:32
	v_mfma_f32_32x32x16_f16 v[16:31], v[52:55], v[92:95], v[16:31]
	v_cvt_pk_f16_f32 v55, v36, v37
	ds_read_b128 v[36:39], v127 offset:10304
	v_cvt_pk_f16_f32 v54, v60, v61
	v_mul_f32_e64 v60, v200, v70
	v_mul_f32_e64 v61, v201, v70
	global_load_dwordx4 v[76:79], v82, s[30:31] offset:64
	global_load_dwordx4 v[32:35], v82, s[30:31] offset:96
	v_pk_fma_f32 v[60:61], v[60:61], v[142:143], v[150:151]
	s_waitcnt vmcnt(11) lgkmcnt(0)
	v_mfma_f32_32x32x16_f16 v[0:15], v[56:59], v[36:39], v[0:15]
	v_mul_f32_e64 v56, v196, v70
	v_mul_f32_e64 v57, v197, v70
	v_mul_f32_e64 v58, v198, v70
	v_mul_f32_e64 v59, v199, v70
	v_cvt_pk_f16_f32 v53, v42, v43
	v_cvt_pk_f16_f32 v52, v40, v41
	global_load_dwordx4 v[40:43], v82, s[30:31] offset:128
	v_mfma_f32_32x32x16_f16 v[16:31], v[44:47], v[36:39], v[16:31]
	s_waitcnt vmcnt(10) lgkmcnt(0)
	v_fma_f32 v38, v56, v146, v166
	v_fma_f32 v39, v57, v147, v167
	v_cvt_pk_f16_f32 v57, v60, v61
	v_mul_f32_e64 v60, v188, v70
	v_mul_f32_e64 v61, v189, v70
	v_cvt_pk_f16_f32 v56, v62, v63
	v_pk_mul_f32 v[62:63], v[124:125], v[70:71] op_sel_hi:[1,0]
	s_waitcnt vmcnt(9) lgkmcnt(0)
	v_pk_fma_f32 v[60:61], v[60:61], v[162:163], v[170:171]
	v_add_co_u32_e32 v170, vcc, s2, v156
	v_mfma_f32_32x32x16_f16 v[0:15], v[64:67], v[84:87], v[0:15]
	v_mul_f32_e64 v64, v192, v70
	v_mul_f32_e64 v65, v193, v70
	v_fma_f32 v36, v58, v144, v164
	v_fma_f32 v37, v59, v145, v165
	v_fma_f32 v136, v64, v160, v168
	v_fma_f32 v137, v65, v161, v169
	s_waitcnt vmcnt(5) lgkmcnt(0)
	v_pk_fma_f32 v[70:71], v[88:89], v[176:177], v[180:181]
	v_pk_fma_f32 v[62:63], v[62:63], v[178:179], v[182:183]
	v_addc_co_u32_e32 v171, vcc, 0, v157, vcc
	v_mfma_f32_32x32x16_f16 v[16:31], v[172:175], v[84:87], v[16:31]
	global_load_dwordx4 v[44:47], v82, s[30:31] offset:160
	v_cvt_pk_f16_f32 v59, v38, v39
	v_cvt_pk_f16_f32 v58, v36, v37
	global_load_dwordx4 v[36:39], v82, s[30:31] offset:192
	v_cvt_pk_f16_f32 v63, v62, v63
	v_cvt_pk_f16_f32 v62, v70, v71
	s_movk_i32 s2, 0x7000
	s_nop 4
	v_add_f32_e32 v64, v0, v16
	v_add_f32_e32 v64, 0, v64
	v_add_f32_e32 v65, v1, v17
	v_add_f32_e32 v64, v65, v64
	v_add_f32_e32 v65, v2, v18
	v_add_f32_e32 v64, v65, v64
	v_add_f32_e32 v65, v3, v19
	v_add_f32_e32 v64, v65, v64
	v_add_f32_e32 v65, v4, v20
	v_add_f32_e32 v64, v65, v64
	v_add_f32_e32 v65, v5, v21
	v_add_f32_e32 v66, v65, v64
	v_pk_add_f32 v[64:65], v[6:7], v[22:23]
	v_add_co_u32_e32 v184, vcc, s2, v156
	v_add_f32_e32 v64, v64, v66
	v_add_f32_e32 v66, v65, v64
	v_pk_add_f32 v[64:65], v[8:9], v[24:25]
	v_addc_co_u32_e32 v185, vcc, 0, v157, vcc
	v_add_f32_e32 v64, v64, v66
	v_add_f32_e32 v66, v65, v64
	v_pk_add_f32 v[64:65], v[10:11], v[26:27]
	s_movk_i32 s2, 0x6000
	v_add_f32_e32 v64, v64, v66
	v_add_f32_e32 v66, v65, v64
	v_pk_add_f32 v[64:65], v[12:13], v[28:29]
	v_add_co_u32_e32 v186, vcc, s2, v156
	v_add_f32_e32 v64, v64, v66
	v_add_f32_e32 v66, v65, v64
	v_pk_add_f32 v[64:65], v[14:15], v[30:31]
	v_addc_co_u32_e32 v187, vcc, 0, v157, vcc
	v_add_f32_e32 v64, v64, v66
	v_add_f32_e32 v69, v65, v64
	ds_bpermute_b32 v84, v209, v69
	global_load_dwordx4 v[64:67], v82, s[30:31] offset:224
	v_cvt_pk_f16_f32 v61, v60, v61
	v_cvt_pk_f16_f32 v60, v136, v137
	s_waitcnt vmcnt(8) lgkmcnt(0)
	v_add_f32_e32 v69, v69, v84
	v_mul_f32_e32 v92, 0x3c800000, v69
	v_ashrrev_i32_e32 v69, 31, v68
	v_lshl_add_u64 v[68:69], v[68:69], 2, s[24:25]
	v_lshl_add_u64 v[124:125], v[68:69], 0, v[82:83]
	global_load_dwordx4 v[140:143], v[124:125], off
	global_load_dwordx4 v[88:91], v[124:125], off offset:32
	global_load_dwordx4 v[84:87], v[124:125], off offset:64
	global_load_dwordx4 v[68:71], v[124:125], off offset:96
	v_pk_add_f32 v[180:181], v[10:11], v[92:93] op_sel_hi:[1,0] neg_lo:[0,1] neg_hi:[0,1]
	v_pk_add_f32 v[182:183], v[8:9], v[92:93] op_sel_hi:[1,0] neg_lo:[0,1] neg_hi:[0,1]
	v_pk_add_f32 v[8:9], v[2:3], v[92:93] op_sel_hi:[1,0] neg_lo:[0,1] neg_hi:[0,1]
	v_pk_add_f32 v[10:11], v[0:1], v[92:93] op_sel_hi:[1,0] neg_lo:[0,1] neg_hi:[0,1]
	ds_read_b128 v[0:3], v253 offset:37504
	v_pk_add_f32 v[178:179], v[12:13], v[92:93] op_sel_hi:[1,0] neg_lo:[0,1] neg_hi:[0,1]
	v_pk_add_f32 v[174:175], v[16:17], v[92:93] op_sel_hi:[1,0] neg_lo:[0,1] neg_hi:[0,1]
	v_fma_f32 v12, v10, v10, 0
	v_fmac_f32_e32 v12, v174, v174
	v_fmac_f32_e32 v12, v11, v11
	v_fmac_f32_e32 v12, v175, v175
	v_pk_add_f32 v[172:173], v[18:19], v[92:93] op_sel_hi:[1,0] neg_lo:[0,1] neg_hi:[0,1]
	v_fmac_f32_e32 v12, v8, v8
	ds_read_b128 v[144:147], v253 offset:20800
	ds_read_b128 v[148:151], v253 offset:22848
	v_fmac_f32_e32 v12, v172, v172
	v_fmac_f32_e32 v12, v9, v9
	v_pk_add_f32 v[4:5], v[4:5], v[92:93] op_sel_hi:[1,0] neg_lo:[0,1] neg_hi:[0,1]
	v_fmac_f32_e32 v12, v173, v173
	v_pk_add_f32 v[168:169], v[20:21], v[92:93] op_sel_hi:[1,0] neg_lo:[0,1] neg_hi:[0,1]
	v_fmac_f32_e32 v12, v4, v4
	v_fmac_f32_e32 v12, v168, v168
	v_fmac_f32_e32 v12, v5, v5
	v_pk_add_f32 v[6:7], v[6:7], v[92:93] op_sel_hi:[1,0] neg_lo:[0,1] neg_hi:[0,1]
	v_fmac_f32_e32 v12, v169, v169
	v_pk_add_f32 v[166:167], v[22:23], v[92:93] op_sel_hi:[1,0] neg_lo:[0,1] neg_hi:[0,1]
	v_fmac_f32_e32 v12, v6, v6
	v_fmac_f32_e32 v12, v166, v166
	v_fmac_f32_e32 v12, v7, v7
	v_fmac_f32_e32 v12, v167, v167
	v_pk_add_f32 v[164:165], v[24:25], v[92:93] op_sel_hi:[1,0] neg_lo:[0,1] neg_hi:[0,1]
	v_fmac_f32_e32 v12, v182, v182
	v_fmac_f32_e32 v12, v164, v164
	v_fmac_f32_e32 v12, v183, v183
	v_fmac_f32_e32 v12, v165, v165
	v_pk_add_f32 v[162:163], v[26:27], v[92:93] op_sel_hi:[1,0] neg_lo:[0,1] neg_hi:[0,1]
	v_fmac_f32_e32 v12, v180, v180
	v_fmac_f32_e32 v12, v162, v162
	v_fmac_f32_e32 v12, v181, v181
	v_fmac_f32_e32 v12, v163, v163
	v_pk_add_f32 v[160:161], v[28:29], v[92:93] op_sel_hi:[1,0] neg_lo:[0,1] neg_hi:[0,1]
	v_fmac_f32_e32 v12, v178, v178
	v_fmac_f32_e32 v12, v160, v160
	v_pk_add_f32 v[154:155], v[30:31], v[92:93] op_sel_hi:[1,0] neg_lo:[0,1] neg_hi:[0,1]
	v_pk_add_f32 v[176:177], v[14:15], v[92:93] op_sel_hi:[1,0] neg_lo:[0,1] neg_hi:[0,1]
	v_fmac_f32_e32 v12, v179, v179
	ds_read_b128 v[92:95], v253 offset:24896
	global_load_dwordx4 v[28:31], v[124:125], off offset:128
	global_load_dwordx4 v[20:23], v[124:125], off offset:160
	v_fmac_f32_e32 v12, v161, v161
	v_fmac_f32_e32 v12, v176, v176
	ds_read_b128 v[120:123], v253 offset:26944
	v_fmac_f32_e32 v12, v154, v154
	v_fmac_f32_e32 v12, v177, v177
	v_fmac_f32_e32 v12, v155, v155
	ds_bpermute_b32 v13, v209, v12
	s_waitcnt vmcnt(14) lgkmcnt(0)
	v_add_f32_e32 v12, v12, v13
	v_fmac_f32_e32 v126, 0x3c800000, v12
	v_mul_f32_e32 v12, 0x4f800000, v126
	v_cmp_gt_f32_e32 vcc, s8, v126
	s_nop 1
	v_cndmask_b32_e32 v12, v126, v12, vcc
	global_load_dwordx4 v[24:27], v[124:125], off offset:192
	global_load_dwordx4 v[16:19], v[124:125], off offset:224
	s_nop 0
	ds_read_b128 v[124:127], v253 offset:28992
	ds_read_b128 v[128:131], v253 offset:31040
	v_sqrt_f32_e32 v13, v12
	s_nop 0
	v_add_u32_e32 v14, -1, v13
	v_fma_f32 v15, -v14, v13, v12
	v_cmp_ge_f32_e64 s[2:3], 0, v15
	v_add_u32_e32 v15, 1, v13
	s_nop 0
	v_cndmask_b32_e64 v14, v13, v14, s[2:3]
	v_fma_f32 v13, -v15, v13, v12
	v_cmp_lt_f32_e64 s[2:3], 0, v13
	s_nop 1
	v_cndmask_b32_e64 v13, v14, v15, s[2:3]
	v_mul_f32_e32 v14, 0x37800000, v13
	s_mov_b32 s2, 0x8000
	v_cndmask_b32_e32 v13, v13, v14, vcc
	v_add_co_u32_e32 v188, vcc, s2, v156
	s_nop 1
	v_addc_co_u32_e32 v189, vcc, 0, v157, vcc
	v_cmp_class_f32_e32 vcc, v12, v208
	ds_read_b128 v[132:135], v253 offset:33088
	ds_read_b128 v[136:139], v253 offset:35456
	v_cndmask_b32_e32 v12, v13, v12, vcc
	v_div_scale_f32 v13, s[2:3], v12, v12, 1.0
	v_rcp_f32_e32 v14, v13
	s_mov_b32 s2, 0x9000
	s_mov_b32 s3, 0xbc90
	v_fma_f32 v15, -v13, v14, 1.0
	v_fmac_f32_e32 v14, v15, v14
	v_div_scale_f32 v15, vcc, 1.0, v12, 1.0
	v_mul_f32_e32 v82, v15, v14
	v_fma_f32 v190, -v13, v82, v15
	v_fmac_f32_e32 v82, v190, v14
	v_fma_f32 v13, -v13, v82, v15
	v_div_fmas_f32 v13, v13, v14, v82
	v_div_fixup_f32 v82, v13, v12, 1.0
	v_pk_mul_f32 v[190:191], v[6:7], v[82:83] op_sel_hi:[1,0]
	v_pk_mul_f32 v[192:193], v[4:5], v[82:83] op_sel_hi:[1,0]
	v_pk_mul_f32 v[4:5], v[8:9], v[82:83] op_sel_hi:[1,0]
	v_pk_mul_f32 v[6:7], v[10:11], v[82:83] op_sel_hi:[1,0]
	s_waitcnt vmcnt(7) lgkmcnt(4)
	v_pk_fma_f32 v[118:119], v[4:5], v[118:119], v[142:143]
	v_pk_fma_f32 v[116:117], v[6:7], v[116:117], v[140:141]
	s_waitcnt vmcnt(4) lgkmcnt(4)
	v_mfma_f32_32x32x16_f16 v[0:15], v[0:3], v[96:99], 0
	v_fma_f32 v72, v192, v72, v88
	v_fma_f32 v73, v193, v73, v89
	v_fma_f32 v74, v190, v74, v90
	v_fma_f32 v75, v191, v75, v91
	ds_read_b128 v[88:91], v253 offset:21824
	v_cvt_pk_f16_f32 v75, v74, v75
	v_cvt_pk_f16_f32 v74, v72, v73
	v_cvt_pk_f16_f32 v73, v118, v119
	v_pk_mul_f32 v[118:119], v[178:179], v[82:83] op_sel_hi:[1,0]
	s_waitcnt vmcnt(4) lgkmcnt(5)
	v_mfma_f32_32x32x16_f16 v[0:15], v[144:147], v[104:107], v[0:15]
	v_mul_f32_e64 v144, v180, v82
	v_mul_f32_e64 v145, v181, v82
	v_mul_f32_e64 v146, v182, v82
	v_mul_f32_e64 v147, v183, v82
	v_fma_f32 v144, v144, v78, v86
	v_fma_f32 v145, v145, v79, v87
	v_pk_fma_f32 v[146:147], v[146:147], v[76:77], v[84:85]
	ds_read_b128 v[84:87], v253 offset:23872
	v_add_co_u32_e32 v152, vcc, s2, v156
	s_waitcnt vmcnt(4) lgkmcnt(6)
	v_mfma_f32_32x32x16_f16 v[0:15], v[148:151], v[100:103], v[0:15]
	v_addc_co_u32_e32 v153, vcc, 0, v157, vcc
	v_fma_f32 v32, v118, v32, v68
	v_fma_f32 v33, v119, v33, v69
	v_cvt_pk_f16_f32 v69, v144, v145
	v_cvt_pk_f16_f32 v68, v146, v147
	ds_read_b128 v[144:147], v253 offset:27968
	ds_read_b128 v[148:151], v253 offset:32064
	s_waitcnt vmcnt(4) lgkmcnt(8)
	v_mfma_f32_32x32x16_f16 v[0:15], v[92:95], v[112:115], v[0:15]
	ds_read_b128 v[92:95], v253 offset:38528
	ds_read_b128 v[76:79], v253 offset:44672
	v_cvt_pk_f16_f32 v72, v116, v117
	v_mul_f32_e64 v116, v176, v82
	v_mul_f32_e64 v117, v177, v82
	v_pk_mul_f32 v[118:119], v[174:175], v[82:83] op_sel_hi:[1,0]
	v_pk_fma_f32 v[34:35], v[116:117], v[34:35], v[70:71]
	v_pk_mul_f32 v[116:117], v[172:173], v[82:83] op_sel_hi:[1,0]
	s_waitcnt vmcnt(2) lgkmcnt(10)
	v_mfma_f32_32x32x16_f16 v[0:15], v[120:123], v[108:111], v[0:15]
	ds_read_b128 v[120:123], v253 offset:30016
	v_fma_f32 v28, v118, v40, v28
	v_fma_f32 v29, v119, v41, v29
	v_fma_f32 v30, v116, v42, v30
	v_fma_f32 v31, v117, v43, v31
	v_cvt_pk_f16_f32 v40, v28, v29
	v_cvt_pk_f16_f32 v41, v30, v31
	v_pk_mul_f32 v[28:29], v[162:163], v[82:83] op_sel_hi:[1,0]
	v_pk_mul_f32 v[30:31], v[164:165], v[82:83] op_sel_hi:[1,0]
	s_waitcnt vmcnt(0) lgkmcnt(10)
	v_mfma_f32_32x32x16_f16 v[0:15], v[124:127], v[48:51], v[0:15]
	v_fma_f32 v24, v30, v36, v24
	v_fma_f32 v25, v31, v37, v25
	v_fma_f32 v26, v28, v38, v26
	v_fma_f32 v27, v29, v39, v27
	ds_read_b128 v[36:39], v253 offset:34112
	v_cvt_pk_f16_f32 v71, v34, v35
	v_cvt_pk_f16_f32 v70, v32, v33
	v_pk_mul_f32 v[32:33], v[166:167], v[82:83] op_sel_hi:[1,0]
	v_pk_mul_f32 v[34:35], v[168:169], v[82:83] op_sel_hi:[1,0]
	s_waitcnt vmcnt(0) lgkmcnt(10)
	v_mfma_f32_32x32x16_f16 v[0:15], v[128:131], v[52:55], v[0:15]
	ds_read_b128 v[126:129], v253 offset:25920
	v_fma_f32 v20, v34, v44, v20
	v_fma_f32 v21, v35, v45, v21
	v_fma_f32 v22, v32, v46, v22
	v_fma_f32 v23, v33, v47, v23
	v_cvt_pk_f16_f32 v42, v20, v21
	v_cvt_pk_f16_f32 v43, v22, v23
	v_pk_mul_f32 v[20:21], v[154:155], v[82:83] op_sel_hi:[1,0]
	v_pk_mul_f32 v[22:23], v[160:161], v[82:83] op_sel_hi:[1,0]
	s_waitcnt vmcnt(0) lgkmcnt(10)
	v_mfma_f32_32x32x16_f16 v[0:15], v[132:135], v[56:59], v[0:15]
	v_fma_f32 v16, v22, v64, v16
	v_fma_f32 v17, v23, v65, v17
	v_fma_f32 v18, v20, v66, v18
	v_fma_f32 v19, v21, v67, v19
	ds_read_b128 v[64:67], v253 offset:36480
	s_mov_b32 s2, 0xa714
	v_mov_b32_e32 v164, 0xb7d0
	v_cvt_pk_f16_f32 v34, v16, v17
	v_cvt_pk_f16_f32 v35, v18, v19
	s_waitcnt vmcnt(0) lgkmcnt(10)
	v_mfma_f32_32x32x16_f16 v[0:15], v[136:139], v[60:63], v[0:15]
	v_cvt_pk_f16_f32 v33, v26, v27
	v_cvt_pk_f16_f32 v32, v24, v25
	ds_read_b128 v[132:135], v253 offset:39552
	v_add_co_u32_e32 v136, vcc, s6, v156
	ds_read_b128 v[140:143], v253 offset:41600
	ds_read_b128 v[44:47], v253 offset:40576
	s_nop 5
	v_cvt_pk_f16_f32 v0, v0, v1
	v_and_b32_e32 v1, 0x7fff7fff, v0
	v_cvt_pk_f16_f32 v2, v2, v3
	v_pk_fma_f16 v16, v1, s2, v164 op_sel_hi:[1,0,0]
	v_and_b32_e32 v3, 0x7fff7fff, v2
	v_pk_fma_f16 v16, v16, v1, s3 op_sel_hi:[1,1,0]
	v_pk_fma_f16 v18, v3, s2, v164 op_sel_hi:[1,0,0]
	v_pk_mul_f16 v16, v1, v16
	v_pk_fma_f16 v18, v18, v3, s3 op_sel_hi:[1,1,0]
	v_exp_f16_e32 v17, v16
	v_exp_f16_sdwa v16, v16 dst_sel:DWORD dst_unused:UNUSED_PAD src0_sel:WORD_1
	v_pk_mul_f16 v18, v3, v18
	v_pk_add_f16 v0, v1, v0
	v_exp_f16_e32 v19, v18
	v_exp_f16_sdwa v18, v18 dst_sel:DWORD dst_unused:UNUSED_PAD src0_sel:WORD_1
	v_pack_b32_f16 v16, v17, v16
	v_pk_fma_f16 v116, v1, v16, v0 neg_lo:[1,0,0] neg_hi:[1,0,0]
	v_pk_add_f16 v1, v3, v2
	v_pack_b32_f16 v0, v19, v18
	v_pk_fma_f16 v117, v3, v0, v1 neg_lo:[1,0,0] neg_hi:[1,0,0]
	v_cvt_pk_f16_f32 v0, v4, v5
	v_and_b32_e32 v1, 0x7fff7fff, v0
	v_pk_fma_f16 v2, v1, s2, v164 op_sel_hi:[1,0,0]
	s_waitcnt vmcnt(0) lgkmcnt(8)
	v_mfma_f32_32x32x16_f16 v[16:31], v[92:95], v[96:99], 0
	v_pk_fma_f16 v2, v2, v1, s3 op_sel_hi:[1,1,0]
	v_cvt_pk_f16_f32 v4, v6, v7
	v_pk_mul_f16 v2, v1, v2
	v_and_b32_e32 v5, 0x7fff7fff, v4
	v_exp_f16_e32 v3, v2
	v_exp_f16_sdwa v2, v2 dst_sel:DWORD dst_unused:UNUSED_PAD src0_sel:WORD_1
	v_pk_fma_f16 v6, v5, s2, v164 op_sel_hi:[1,0,0]
	v_pk_add_f16 v0, v1, v0
	v_pk_fma_f16 v6, v6, v5, s3 op_sel_hi:[1,1,0]
	v_pack_b32_f16 v2, v3, v2
	v_pk_mul_f16 v6, v5, v6
	v_pk_fma_f16 v118, v1, v2, v0 neg_lo:[1,0,0] neg_hi:[1,0,0]
	v_cvt_pk_f16_f32 v1, v8, v9
	v_exp_f16_e32 v7, v6
	v_exp_f16_sdwa v6, v6 dst_sel:DWORD dst_unused:UNUSED_PAD src0_sel:WORD_1
	v_and_b32_e32 v2, 0x7fff7fff, v1
	v_pk_fma_f16 v3, v2, s2, v164 op_sel_hi:[1,0,0]
	v_mfma_f32_32x32x16_f16 v[16:31], v[88:91], v[104:107], v[16:31]
	v_pk_fma_f16 v3, v3, v2, s3 op_sel_hi:[1,1,0]
	v_pack_b32_f16 v0, v7, v6
	v_pk_mul_f16 v3, v2, v3
	v_pk_add_f16 v4, v5, v4
	v_exp_f16_e32 v6, v3
	v_exp_f16_sdwa v3, v3 dst_sel:DWORD dst_unused:UNUSED_PAD src0_sel:WORD_1
	v_pk_fma_f16 v119, v5, v0, v4 neg_lo:[1,0,0] neg_hi:[1,0,0]
	v_cvt_pk_f16_f32 v4, v10, v11
	v_pk_add_f16 v1, v2, v1
	v_pack_b32_f16 v0, v6, v3
	v_and_b32_e32 v5, 0x7fff7fff, v4
	v_pk_fma_f16 v124, v2, v0, v1 neg_lo:[1,0,0] neg_hi:[1,0,0]
	v_pk_fma_f16 v0, v5, s2, v164 op_sel_hi:[1,0,0]
	v_mfma_f32_32x32x16_f16 v[16:31], v[84:87], v[100:103], v[16:31]
	v_pk_fma_f16 v0, v0, v5, s3 op_sel_hi:[1,1,0]
	v_addc_co_u32_e32 v137, vcc, 0, v157, vcc
	v_pk_mul_f16 v0, v5, v0
	ds_read_b128 v[84:87], v253 offset:43648
	v_exp_f16_e32 v6, v0
	v_exp_f16_sdwa v7, v0 dst_sel:DWORD dst_unused:UNUSED_PAD src0_sel:WORD_1
	ds_read_b128 v[0:3], v254 offset:3072
	s_waitcnt vmcnt(0) lgkmcnt(6)
	v_mfma_f32_32x32x16_f16 v[16:31], v[126:129], v[112:115], v[16:31]
	s_mov_b32 s6, 0xb000
	v_cvt_pk_f16_f32 v8, v12, v13
	v_and_b32_e32 v9, 0x7fff7fff, v8
	v_pk_fma_f16 v10, v9, s2, v164 op_sel_hi:[1,0,0]
	v_pack_b32_f16 v6, v6, v7
	v_pk_fma_f16 v10, v10, v9, s3 op_sel_hi:[1,1,0]
	v_pk_add_f16 v4, v5, v4
	v_mfma_f32_32x32x16_f16 v[16:31], v[144:147], v[108:111], v[16:31]
	v_pk_mul_f16 v10, v9, v10
	v_pk_fma_f16 v125, v5, v6, v4 neg_lo:[1,0,0] neg_hi:[1,0,0]
	v_exp_f16_e32 v11, v10
	v_exp_f16_sdwa v10, v10 dst_sel:DWORD dst_unused:UNUSED_PAD src0_sel:WORD_1
	v_pk_add_f16 v5, v9, v8
	v_pack_b32_f16 v4, v11, v10
	v_mfma_f32_32x32x16_f16 v[16:31], v[120:123], v[48:51], v[16:31]
	v_pk_fma_f16 v126, v9, v4, v5 neg_lo:[1,0,0] neg_hi:[1,0,0]
	v_cvt_pk_f16_f32 v4, v14, v15
	v_and_b32_e32 v5, 0x7fff7fff, v4
	v_pk_fma_f16 v6, v5, s2, v164 op_sel_hi:[1,0,0]
	v_pk_add_f16 v4, v5, v4
	v_pk_fma_f16 v6, v6, v5, s3 op_sel_hi:[1,1,0]
	v_mfma_f32_32x32x16_f16 v[16:31], v[148:151], v[52:55], v[16:31]
	v_add_co_u32_e32 v150, vcc, s7, v156
	v_pk_mul_f16 v6, v5, v6
	s_nop 0
	v_addc_co_u32_e32 v151, vcc, 0, v157, vcc
	ds_read_b128 v[88:91], v253 offset:45696
	v_add_co_u32_e32 v152, vcc, s6, v156
	v_mfma_f32_32x32x16_f16 v[16:31], v[36:39], v[56:59], v[16:31]
	s_nop 0
	v_addc_co_u32_e32 v153, vcc, 0, v157, vcc
	ds_read_b128 v[92:95], v253 offset:47744
	ds_read_b128 v[146:149], v253 offset:48768
	ds_read_b128 v[120:123], v253 offset:51840
	ds_read_b128 v[166:169], v253 offset:50816
	v_exp_f16_e32 v7, v6
	s_waitcnt vmcnt(0) lgkmcnt(10)
	v_mfma_f32_32x32x16_f16 v[16:31], v[64:67], v[60:63], v[16:31]
	ds_read_b128 v[64:67], v253 offset:49792
	v_exp_f16_sdwa v6, v6 dst_sel:DWORD dst_unused:UNUSED_PAD src0_sel:WORD_1
	s_mov_b32 s6, 0xe000
	v_add_co_u32_e32 v138, vcc, s6, v156
	v_pack_b32_f16 v6, v7, v6
	v_pk_fma_f16 v127, v5, v6, v4 neg_lo:[1,0,0] neg_hi:[1,0,0]
	s_nop 5
	v_cvt_pk_f16_f32 v8, v16, v17
	v_and_b32_e32 v9, 0x7fff7fff, v8
	v_pk_fma_f16 v10, v9, s2, v164 op_sel_hi:[1,0,0]
	v_pk_add_f16 v5, v9, v8
	v_pk_fma_f16 v10, v10, v9, s3 op_sel_hi:[1,1,0]
	v_addc_co_u32_e32 v139, vcc, 0, v157, vcc
	v_pk_mul_f16 v10, v9, v10
	v_cvt_pk_f16_f32 v8, v20, v21
	v_exp_f16_e32 v11, v10
	v_exp_f16_sdwa v10, v10 dst_sel:DWORD dst_unused:UNUSED_PAD src0_sel:WORD_1
	v_and_b32_e32 v20, 0x7fff7fff, v8
	v_pk_add_f16 v82, v20, v8
	ds_read_b128 v[36:39], v254 offset:2048
	v_pack_b32_f16 v4, v11, v10
	v_pk_fma_f16 v128, v9, v4, v5 neg_lo:[1,0,0] neg_hi:[1,0,0]
	v_cvt_pk_f16_f32 v4, v18, v19
	ds_read_b128 v[16:19], v254 offset:1024
	v_and_b32_e32 v5, 0x7fff7fff, v4
	v_pk_fma_f16 v6, v5, s2, v164 op_sel_hi:[1,0,0]
	v_pk_fma_f16 v9, v20, s2, v164 op_sel_hi:[1,0,0]
	v_pk_fma_f16 v6, v6, v5, s3 op_sel_hi:[1,1,0]
	v_pk_fma_f16 v9, v9, v20, s3 op_sel_hi:[1,1,0]
	v_pk_mul_f16 v6, v5, v6
	v_pk_mul_f16 v9, v20, v9
	v_exp_f16_e32 v7, v6
	v_exp_f16_sdwa v6, v6 dst_sel:DWORD dst_unused:UNUSED_PAD src0_sel:WORD_1
	v_exp_f16_e32 v10, v9
	v_exp_f16_sdwa v9, v9 dst_sel:DWORD dst_unused:UNUSED_PAD src0_sel:WORD_1
	v_pk_add_f16 v4, v5, v4
	v_pack_b32_f16 v6, v7, v6
	v_pk_fma_f16 v129, v5, v6, v4 neg_lo:[1,0,0] neg_hi:[1,0,0]
	v_pack_b32_f16 v21, v10, v9
	s_waitcnt vmcnt(0) lgkmcnt(8)
	v_mfma_f32_32x32x16_f16 v[0:15], v[0:3], v[96:99], 0
	v_pk_fma_f16 v130, v20, v21, v82 neg_lo:[1,0,0] neg_hi:[1,0,0]
	v_cvt_pk_f16_f32 v82, v22, v23
	v_and_b32_e32 v131, 0x7fff7fff, v82
	v_pk_fma_f16 v20, v131, s2, v164 op_sel_hi:[1,0,0]
	v_cvt_pk_f16_f32 v24, v24, v25
	v_pk_fma_f16 v20, v20, v131, s3 op_sel_hi:[1,1,0]
	v_and_b32_e32 v25, 0x7fff7fff, v24
	v_pk_mul_f16 v20, v131, v20
	v_mfma_f32_32x32x16_f16 v[0:15], v[132:135], v[104:107], v[0:15]
	v_exp_f16_e32 v144, v20
	v_exp_f16_sdwa v132, v20 dst_sel:DWORD dst_unused:UNUSED_PAD src0_sel:WORD_1
	v_pk_fma_f16 v20, v25, s2, v164 op_sel_hi:[1,0,0]
	ds_read_b128 v[152:155], v253 offset:46720
	v_pk_fma_f16 v20, v20, v25, s3 op_sel_hi:[1,1,0]
	v_pack_b32_f16 v132, v144, v132
	v_pk_mul_f16 v133, v25, v20
	ds_read_b128 v[20:23], v254 offset:4096
	v_mfma_f32_32x32x16_f16 v[0:15], v[140:143], v[100:103], v[0:15]
	ds_read_b128 v[142:145], v253 offset:42624
	v_cvt_pk_f16_f32 v26, v26, v27
	v_and_b32_e32 v27, 0x7fff7fff, v26
	v_exp_f16_e32 v134, v133
	v_exp_f16_sdwa v133, v133 dst_sel:DWORD dst_unused:UNUSED_PAD src0_sel:WORD_1
	v_pk_add_f16 v82, v131, v82
	v_pk_add_f16 v24, v25, v24
	v_mfma_f32_32x32x16_f16 v[0:15], v[84:87], v[112:115], v[0:15]
	v_pk_fma_f16 v84, v27, s2, v164 op_sel_hi:[1,0,0]
	v_pk_fma_f16 v131, v131, v132, v82 neg_lo:[1,0,0] neg_hi:[1,0,0]
	v_pk_fma_f16 v84, v84, v27, s3 op_sel_hi:[1,1,0]
	v_pack_b32_f16 v82, v134, v133
	v_pk_mul_f16 v84, v27, v84
	v_pk_fma_f16 v132, v25, v82, v24 neg_lo:[1,0,0] neg_hi:[1,0,0]
	v_exp_f16_e32 v85, v84
	s_waitcnt vmcnt(0) lgkmcnt(10)
	v_mfma_f32_32x32x16_f16 v[0:15], v[88:91], v[108:111], v[0:15]
	v_exp_f16_sdwa v84, v84 dst_sel:DWORD dst_unused:UNUSED_PAD src0_sel:WORD_1
	v_pk_add_f16 v25, v27, v26
	ds_read_b128 v[170:173], v254
	s_mov_b32 s6, 0x13000
	v_pack_b32_f16 v24, v85, v84
	v_pk_fma_f16 v133, v27, v24, v25 neg_lo:[1,0,0] neg_hi:[1,0,0]
	v_cvt_pk_f16_f32 v24, v28, v29
	s_waitcnt vmcnt(0) lgkmcnt(10)
	v_mfma_f32_32x32x16_f16 v[0:15], v[92:95], v[72:75], v[0:15]
	v_and_b32_e32 v25, 0x7fff7fff, v24
	v_cvt_pk_f16_f32 v28, v30, v31
	v_pk_fma_f16 v26, v25, s2, v164 op_sel_hi:[1,0,0]
	v_and_b32_e32 v29, 0x7fff7fff, v28
	v_pk_fma_f16 v26, v26, v25, s3 op_sel_hi:[1,1,0]
	v_pk_fma_f16 v30, v29, s2, v164 op_sel_hi:[1,0,0]
	v_pk_mul_f16 v26, v25, v26
	s_waitcnt vmcnt(0) lgkmcnt(6)
	v_mfma_f32_32x32x16_f16 v[0:15], v[64:67], v[68:71], v[0:15]
	v_pk_fma_f16 v30, v30, v29, s3 op_sel_hi:[1,1,0]
	v_exp_f16_e32 v27, v26
	v_exp_f16_sdwa v26, v26 dst_sel:DWORD dst_unused:UNUSED_PAD src0_sel:WORD_1
	v_pk_mul_f16 v30, v29, v30
	v_pk_add_f16 v24, v25, v24
	v_exp_f16_e32 v31, v30
	v_exp_f16_sdwa v30, v30 dst_sel:DWORD dst_unused:UNUSED_PAD src0_sel:WORD_1
	v_mfma_f32_32x32x16_f16 v[0:15], v[120:123], v[40:43], v[0:15]
	v_pack_b32_f16 v26, v27, v26
	v_pk_fma_f16 v134, v25, v26, v24 neg_lo:[1,0,0] neg_hi:[1,0,0]
	v_pack_b32_f16 v24, v31, v30
	v_pk_add_f16 v25, v29, v28
	v_add_co_u32_e32 v150, vcc, s6, v156
	v_pk_fma_f16 v135, v29, v24, v25 neg_lo:[1,0,0] neg_hi:[1,0,0]
	s_waitcnt vmcnt(0) lgkmcnt(4)
	v_mfma_f32_32x32x16_f16 v[0:15], v[16:19], v[32:35], v[0:15]
	v_addc_co_u32_e32 v151, vcc, 0, v157, vcc
	ds_read_b128 v[64:67], v254 offset:5120
	ds_read_b128 v[84:87], v254 offset:7168
	s_mov_b32 s6, 0x10000
	v_add_co_u32_e32 v140, vcc, s6, v156
	s_nop 6
	v_cvt_pk_f16_f32 v16, v0, v1
	v_and_b32_e32 v17, 0x7fff7fff, v16
	v_pk_fma_f16 v0, v17, s2, v164 op_sel_hi:[1,0,0]
	v_cvt_pk_f16_f32 v24, v2, v3
	v_pk_fma_f16 v0, v0, v17, s3 op_sel_hi:[1,1,0]
	v_and_b32_e32 v25, 0x7fff7fff, v24
	v_pk_mul_f16 v0, v17, v0
	v_pk_add_f16 v16, v17, v16
	v_exp_f16_e32 v18, v0
	v_exp_f16_sdwa v19, v0 dst_sel:DWORD dst_unused:UNUSED_PAD src0_sel:WORD_1
	v_pk_fma_f16 v0, v25, s2, v164 op_sel_hi:[1,0,0]
	v_addc_co_u32_e32 v141, vcc, 0, v157, vcc
	v_pk_fma_f16 v0, v0, v25, s3 op_sel_hi:[1,1,0]
	v_pack_b32_f16 v18, v18, v19
	v_pk_mul_f16 v26, v25, v0
	ds_read_b128 v[0:3], v254 offset:21824
	v_exp_f16_e32 v27, v26
	v_exp_f16_sdwa v26, v26 dst_sel:DWORD dst_unused:UNUSED_PAD src0_sel:WORD_1
	v_pk_fma_f16 v120, v17, v18, v16 neg_lo:[1,0,0] neg_hi:[1,0,0]
	v_pk_add_f16 v17, v25, v24
	ds_read_b128 v[88:91], v254 offset:9216
	v_pack_b32_f16 v16, v27, v26
	v_pk_fma_f16 v121, v25, v16, v17 neg_lo:[1,0,0] neg_hi:[1,0,0]
	s_waitcnt vmcnt(0) lgkmcnt(6)
	v_mfma_f32_32x32x16_f16 v[16:31], v[20:23], v[96:99], 0
	v_cvt_pk_f16_f32 v82, v4, v5
	s_mov_b32 s6, 0xf000
	v_and_b32_e32 v122, 0x7fff7fff, v82
	v_add_co_u32_e32 v162, vcc, s6, v156
	v_pk_fma_f16 v4, v122, s2, v164 op_sel_hi:[1,0,0]
	s_nop 0
	v_addc_co_u32_e32 v163, vcc, 0, v157, vcc
	v_mfma_f32_32x32x16_f16 v[16:31], v[44:47], v[104:107], v[16:31]
	v_pk_fma_f16 v4, v4, v122, s3 op_sel_hi:[1,1,0]
	ds_read_b128 v[92:95], v254 offset:11264
	v_pk_mul_f16 v4, v122, v4
	v_cvt_pk_f16_f32 v45, v6, v7
	v_exp_f16_e32 v5, v4
	v_exp_f16_sdwa v4, v4 dst_sel:DWORD dst_unused:UNUSED_PAD src0_sel:WORD_1
	v_and_b32_e32 v46, 0x7fff7fff, v45
	s_waitcnt vmcnt(0) lgkmcnt(6)
	v_mfma_f32_32x32x16_f16 v[16:31], v[142:145], v[100:103], v[16:31]
	s_mov_b32 s6, 0x11000
	v_pack_b32_f16 v44, v5, v4
	v_pk_fma_f16 v4, v46, s2, v164 op_sel_hi:[1,0,0]
	v_cvt_pk_f16_f32 v10, v10, v11
	v_pk_fma_f16 v4, v4, v46, s3 op_sel_hi:[1,1,0]
	v_and_b32_e32 v11, 0x7fff7fff, v10
	v_pk_mul_f16 v47, v46, v4
	v_mfma_f32_32x32x16_f16 v[16:31], v[76:79], v[112:115], v[16:31]
	ds_read_b128 v[4:7], v254 offset:13312
	v_exp_f16_e32 v76, v47
	v_exp_f16_sdwa v47, v47 dst_sel:DWORD dst_unused:UNUSED_PAD src0_sel:WORD_1
	v_pk_add_f16 v77, v122, v82
	v_pk_add_f16 v45, v46, v45
	v_pk_fma_f16 v122, v122, v44, v77 neg_lo:[1,0,0] neg_hi:[1,0,0]
	v_pack_b32_f16 v44, v76, v47
	v_mfma_f32_32x32x16_f16 v[16:31], v[152:155], v[108:111], v[16:31]
	ds_read_b128 v[76:79], v254 offset:15360
	v_cvt_pk_f16_f32 v47, v8, v9
	v_add_co_u32_e32 v8, vcc, s6, v156
	v_and_b32_e32 v82, 0x7fff7fff, v47
	s_nop 0
	v_addc_co_u32_e32 v9, vcc, 0, v157, vcc
	v_mfma_f32_32x32x16_f16 v[16:31], v[146:149], v[72:75], v[16:31]
	ds_read_b128 v[72:75], v254 offset:17728
	v_pk_fma_f16 v123, v82, s2, v164 op_sel_hi:[1,0,0]
	s_mov_b32 s6, 0x12000
	v_pk_fma_f16 v123, v123, v82, s3 op_sel_hi:[1,1,0]
	v_add_co_u32_e32 v160, vcc, s6, v156
	ds_read_b128 v[146:149], v254 offset:6144
	v_mfma_f32_32x32x16_f16 v[16:31], v[166:169], v[68:71], v[16:31]
	v_pk_mul_f16 v68, v82, v123
	v_addc_co_u32_e32 v161, vcc, 0, v157, vcc
	v_exp_f16_e32 v136, v68
	v_exp_f16_sdwa v137, v68 dst_sel:DWORD dst_unused:UNUSED_PAD src0_sel:WORD_1
	ds_read_b128 v[68:71], v254 offset:19776
	ds_read_b128 v[142:145], v254 offset:22848
	s_waitcnt vmcnt(0) lgkmcnt(11)
	v_mfma_f32_32x32x16_f16 v[16:31], v[170:173], v[40:43], v[16:31]
	v_pk_fma_f16 v123, v46, v44, v45 neg_lo:[1,0,0] neg_hi:[1,0,0]
	v_pack_b32_f16 v136, v136, v137
	v_pk_add_f16 v137, v82, v47
	ds_read_b128 v[170:173], v254 offset:16384
	v_pk_fma_f16 v136, v82, v136, v137 neg_lo:[1,0,0] neg_hi:[1,0,0]
	s_mov_b32 s6, 0x16000
	ds_read_b128 v[152:155], v254 offset:25920
	v_mfma_f32_32x32x16_f16 v[16:31], v[36:39], v[32:35], v[16:31]
	v_pk_fma_f16 v32, v11, s2, v164 op_sel_hi:[1,0,0]
	s_nop 0
	v_pk_fma_f16 v32, v32, v11, s3 op_sel_hi:[1,1,0]
	s_nop 0
	v_pk_mul_f16 v32, v11, v32
	s_nop 6
	v_cvt_pk_f16_f32 v24, v24, v25
	v_exp_f16_e32 v165, v32
	v_exp_f16_sdwa v166, v32 dst_sel:DWORD dst_unused:UNUSED_PAD src0_sel:WORD_1
	s_waitcnt vmcnt(0) lgkmcnt(10)
	v_mfma_f32_32x32x16_f16 v[32:47], v[0:3], v[96:99], 0
	v_pk_add_f16 v1, v11, v10
	v_cvt_pk_f16_f32 v10, v14, v15
	v_pack_b32_f16 v0, v165, v166
	ds_read_b128 v[166:169], v254 offset:8192
	v_pk_fma_f16 v137, v11, v0, v1 neg_lo:[1,0,0] neg_hi:[1,0,0]
	v_cvt_pk_f16_f32 v0, v12, v13
	v_and_b32_e32 v1, 0x7fff7fff, v0
	v_mfma_f32_32x32x16_f16 v[32:47], v[64:67], v[104:107], v[32:47]
	ds_read_b128 v[64:67], v254 offset:10240
	v_pk_fma_f16 v2, v1, s2, v164 op_sel_hi:[1,0,0]
	v_and_b32_e32 v11, 0x7fff7fff, v10
	v_pk_fma_f16 v2, v2, v1, s3 op_sel_hi:[1,1,0]
	v_pk_fma_f16 v12, v11, s2, v164 op_sel_hi:[1,0,0]
	v_pk_mul_f16 v2, v1, v2
	v_pk_fma_f16 v12, v12, v11, s3 op_sel_hi:[1,1,0]
	v_mfma_f32_32x32x16_f16 v[32:47], v[84:87], v[100:103], v[32:47]
	v_exp_f16_e32 v3, v2
	v_exp_f16_sdwa v2, v2 dst_sel:DWORD dst_unused:UNUSED_PAD src0_sel:WORD_1
	v_pk_mul_f16 v12, v11, v12
	v_pk_add_f16 v0, v1, v0
	v_exp_f16_e32 v13, v12
	v_exp_f16_sdwa v12, v12 dst_sel:DWORD dst_unused:UNUSED_PAD src0_sel:WORD_1
	v_pack_b32_f16 v2, v3, v2
	s_waitcnt vmcnt(0) lgkmcnt(11)
	v_mfma_f32_32x32x16_f16 v[32:47], v[88:91], v[112:115], v[32:47]
	ds_read_b128 v[88:91], v254 offset:12288
	v_pk_fma_f16 v138, v1, v2, v0 neg_lo:[1,0,0] neg_hi:[1,0,0]
	v_pack_b32_f16 v0, v13, v12
	v_pk_add_f16 v1, v11, v10
	v_add_co_u32_e32 v162, vcc, s6, v156
	v_pk_fma_f16 v139, v11, v0, v1 neg_lo:[1,0,0] neg_hi:[1,0,0]
	s_waitcnt vmcnt(0) lgkmcnt(11)
	v_mfma_f32_32x32x16_f16 v[32:47], v[92:95], v[108:111], v[32:47]
	ds_read_b128 v[92:95], v254 offset:14336
	v_cvt_pk_f16_f32 v0, v16, v17
	v_and_b32_e32 v1, 0x7fff7fff, v0
	v_pk_fma_f16 v2, v1, s2, v164 op_sel_hi:[1,0,0]
	v_pk_add_f16 v0, v1, v0
	v_pk_fma_f16 v2, v2, v1, s3 op_sel_hi:[1,1,0]
	v_addc_co_u32_e32 v163, vcc, 0, v157, vcc
	s_waitcnt vmcnt(0) lgkmcnt(11)
	v_mfma_f32_32x32x16_f16 v[32:47], v[4:7], v[48:51], v[32:47]
	v_cvt_pk_f16_f32 v4, v18, v19
	v_and_b32_e32 v5, 0x7fff7fff, v4
	ds_read_b128 v[16:19], v254 offset:18752
	v_pk_fma_f16 v6, v5, s2, v164 op_sel_hi:[1,0,0]
	v_pk_mul_f16 v2, v1, v2
	v_pk_fma_f16 v6, v6, v5, s3 op_sel_hi:[1,1,0]
	v_exp_f16_e32 v3, v2
	s_waitcnt vmcnt(0) lgkmcnt(11)
	v_mfma_f32_32x32x16_f16 v[32:47], v[76:79], v[52:55], v[32:47]
	v_exp_f16_sdwa v2, v2 dst_sel:DWORD dst_unused:UNUSED_PAD src0_sel:WORD_1
	v_pk_mul_f16 v6, v5, v6
	ds_read_b128 v[84:87], v254 offset:28992
	v_exp_f16_e32 v7, v6
	v_exp_f16_sdwa v6, v6 dst_sel:DWORD dst_unused:UNUSED_PAD src0_sel:WORD_1
	v_pack_b32_f16 v2, v3, v2
	v_pk_fma_f16 v140, v1, v2, v0 neg_lo:[1,0,0] neg_hi:[1,0,0]
	s_waitcnt vmcnt(0) lgkmcnt(11)
	v_mfma_f32_32x32x16_f16 v[32:47], v[72:75], v[56:59], v[32:47]
	v_pack_b32_f16 v0, v7, v6
	ds_read_b128 v[72:75], v254 offset:20800
	v_pk_add_f16 v1, v5, v4
	s_mov_b32 s6, 0x14000
	v_pk_fma_f16 v141, v5, v0, v1 neg_lo:[1,0,0] neg_hi:[1,0,0]
	v_lshlrev_b32_e32 v0, 2, v159
	v_ashrrev_i32_e32 v1, 31, v0
	v_lshl_add_u64 v[0:1], v[0:1], 2, v[80:81]
	global_load_dwordx4 v[76:79], v[0:1], off
	s_waitcnt vmcnt(1) lgkmcnt(10)
	v_mfma_f32_32x32x16_f16 v[32:47], v[68:71], v[60:63], v[32:47]
	ds_read_b128 v[68:71], v254 offset:40576
	ds_read_b128 v[174:177], v254 offset:23872
	s_waitcnt vmcnt(0) lgkmcnt(2)
	v_cvt_pk_f16_f32 v79, v20, v21
	v_and_b32_e32 v80, 0x7fff7fff, v79
	v_pk_fma_f16 v20, v80, s2, v164 op_sel_hi:[1,0,0]
	v_pk_add_f16 v79, v80, v79
	v_pk_fma_f16 v20, v20, v80, s3 op_sel_hi:[1,1,0]
	v_and_b32_e32 v25, 0x7fff7fff, v24
	v_mfma_f32_32x32x16_f16 v[0:15], v[142:145], v[96:99], 0
	v_cvt_pk_f16_f32 v143, v22, v23
	v_pk_mul_f16 v20, v80, v20
	v_and_b32_e32 v144, 0x7fff7fff, v143
	v_exp_f16_e32 v81, v20
	v_exp_f16_sdwa v82, v20 dst_sel:DWORD dst_unused:UNUSED_PAD src0_sel:WORD_1
	v_pk_fma_f16 v20, v144, s2, v164 op_sel_hi:[1,0,0]
	v_cvt_pk_f16_f32 v26, v26, v27
	v_pk_fma_f16 v20, v20, v144, s3 op_sel_hi:[1,1,0]
	v_mfma_f32_32x32x16_f16 v[0:15], v[146:149], v[104:107], v[0:15]
	v_pk_mul_f16 v142, v144, v20
	ds_read_b128 v[20:23], v254 offset:27968
	v_add_co_u32_e32 v148, vcc, s6, v156
	s_mov_b32 s6, 0x15000
	s_nop 0
	v_addc_co_u32_e32 v149, vcc, 0, v157, vcc
	v_mfma_f32_32x32x16_f16 v[0:15], v[166:169], v[100:103], v[0:15]
	ds_read_b128 v[166:169], v254 offset:32064
	ds_read_b128 v[178:181], v254 offset:24896
	v_add_co_u32_e32 v194, vcc, s6, v156
	v_exp_f16_e32 v145, v142
	s_nop 0
	v_addc_co_u32_e32 v195, vcc, 0, v157, vcc
	v_exp_f16_sdwa v146, v142 dst_sel:DWORD dst_unused:UNUSED_PAD src0_sel:WORD_1
	v_mfma_f32_32x32x16_f16 v[0:15], v[64:67], v[112:115], v[0:15]
	ds_read_b128 v[64:67], v254 offset:36480
	v_pack_b32_f16 v81, v81, v82
	v_pk_fma_f16 v142, v80, v81, v79 neg_lo:[1,0,0] neg_hi:[1,0,0]
	v_pack_b32_f16 v79, v145, v146
	v_pk_add_f16 v80, v144, v143
	s_mov_b32 s6, 0x18000
	v_pk_fma_f16 v143, v144, v79, v80 neg_lo:[1,0,0] neg_hi:[1,0,0]
	v_mfma_f32_32x32x16_f16 v[0:15], v[88:91], v[108:111], v[0:15]
	ds_read_b128 v[88:91], v254 offset:41600
	v_pk_fma_f16 v79, v25, s2, v164 op_sel_hi:[1,0,0]
	v_add_co_u32_e32 v160, vcc, s6, v156
	v_pk_fma_f16 v79, v79, v25, s3 op_sel_hi:[1,1,0]
	v_pk_add_f16 v24, v25, v24
	v_pk_mul_f16 v79, v25, v79
	v_mfma_f32_32x32x16_f16 v[0:15], v[92:95], v[48:51], v[0:15]
	ds_read_b128 v[92:95], v254 offset:33088
	ds_read_b128 v[186:189], v254 offset:31040
	v_exp_f16_e32 v48, v79
	v_exp_f16_sdwa v49, v79 dst_sel:DWORD dst_unused:UNUSED_PAD src0_sel:WORD_1
	v_addc_co_u32_e32 v161, vcc, 0, v157, vcc
	v_and_b32_e32 v27, 0x7fff7fff, v26
	v_mfma_f32_32x32x16_f16 v[0:15], v[170:173], v[52:55], v[0:15]
	v_pack_b32_f16 v48, v48, v49
	v_pk_fma_f16 v144, v25, v48, v24 neg_lo:[1,0,0] neg_hi:[1,0,0]
	v_cvt_pk_f16_f32 v25, v28, v29
	v_pk_fma_f16 v50, v27, s2, v164 op_sel_hi:[1,0,0]
	v_mov_b32_e32 v82, v83
	v_pk_fma_f16 v50, v50, v27, s3 op_sel_hi:[1,1,0]
	ds_read_b128 v[170:173], v254 offset:30016
	v_mfma_f32_32x32x16_f16 v[0:15], v[16:19], v[56:59], v[0:15]
	v_pk_mul_f16 v50, v27, v50
	ds_read_b128 v[182:185], v254 offset:34112
	v_exp_f16_e32 v51, v50
	v_exp_f16_sdwa v50, v50 dst_sel:DWORD dst_unused:UNUSED_PAD src0_sel:WORD_1
	v_and_b32_e32 v16, 0x7fff7fff, v25
	v_pk_fma_f16 v17, v16, s2, v164 op_sel_hi:[1,0,0]
	s_mov_b32 s6, 0x17000
	v_mfma_f32_32x32x16_f16 v[0:15], v[72:75], v[60:63], v[0:15]
	ds_read_b128 v[72:75], v254 offset:37504
	v_pack_b32_f16 v24, v51, v50
	v_cvt_pk_f16_f32 v19, v76, v77
	v_cvt_pk_f16_f32 v28, v78, 1.0
	ds_read_b128 v[76:79], v254 offset:42624
	v_cndmask_b32_e64 v80, 0, v19, s[4:5]
	v_cndmask_b32_e64 v81, 0, v28, s[4:5]
	v_pk_fma_f16 v17, v17, v16, s3 op_sel_hi:[1,1,0]
	v_add_co_u32_e32 v202, vcc, s6, v156
	s_waitcnt vmcnt(0) lgkmcnt(12)
	v_mfma_f32_32x32x16_f16 v[48:63], v[68:71], v[80:83], 0
	v_pk_mul_f16 v17, v16, v17
	v_addc_co_u32_e32 v203, vcc, 0, v157, vcc
	v_exp_f16_e32 v18, v17
	v_exp_f16_sdwa v17, v17 dst_sel:DWORD dst_unused:UNUSED_PAD src0_sel:WORD_1
	ds_read_b128 v[190:193], v254 offset:43648
	v_pk_add_f16 v19, v27, v26
	s_waitcnt vmcnt(0) lgkmcnt(12)
	v_mfma_f32_32x32x16_f16 v[48:63], v[174:177], v[116:119], v[48:63]
	v_pk_fma_f16 v145, v27, v24, v19 neg_lo:[1,0,0] neg_hi:[1,0,0]
	v_pack_b32_f16 v17, v18, v17
	v_pk_add_f16 v18, v16, v25
	v_cvt_pk_f16_f32 v19, v30, v31
	v_and_b32_e32 v24, 0x7fff7fff, v19
	v_pk_fma_f16 v146, v16, v17, v18 neg_lo:[1,0,0] neg_hi:[1,0,0]
	v_cvt_pk_f16_f32 v17, v32, v33
	s_waitcnt vmcnt(0) lgkmcnt(11)
	v_mfma_f32_32x32x16_f16 v[48:63], v[20:23], v[124:127], v[48:63]
	v_pk_fma_f16 v25, v24, s2, v164 op_sel_hi:[1,0,0]
	v_and_b32_e32 v32, 0x7fff7fff, v17
	v_pk_fma_f16 v25, v25, v24, s3 op_sel_hi:[1,1,0]
	v_pk_fma_f16 v18, v32, s2, v164 op_sel_hi:[1,0,0]
	v_pk_mul_f16 v25, v24, v25
	v_pk_fma_f16 v18, v18, v32, s3 op_sel_hi:[1,1,0]
	v_exp_f16_e32 v26, v25
	s_waitcnt vmcnt(0) lgkmcnt(10)
	v_mfma_f32_32x32x16_f16 v[48:63], v[166:169], v[128:131], v[48:63]
	ds_read_b128 v[166:169], v254 offset:38528
	v_exp_f16_sdwa v25, v25 dst_sel:DWORD dst_unused:UNUSED_PAD src0_sel:WORD_1
	ds_read_b128 v[174:177], v254 offset:26944
	v_pk_mul_f16 v18, v32, v18
	v_pk_add_f16 v19, v24, v19
	v_exp_f16_e32 v20, v18
	v_exp_f16_sdwa v18, v18 dst_sel:DWORD dst_unused:UNUSED_PAD src0_sel:WORD_1
	v_pack_b32_f16 v16, v26, v25
	v_pk_fma_f16 v147, v24, v16, v19 neg_lo:[1,0,0] neg_hi:[1,0,0]
	s_waitcnt vmcnt(0) lgkmcnt(10)
	v_mfma_f32_32x32x16_f16 v[48:63], v[64:67], v[132:135], v[48:63]
	v_pack_b32_f16 v33, v20, v18
	v_pk_add_f16 v64, v32, v17
	v_cvt_pk_f16_f32 v36, v36, v37
	v_pk_fma_f16 v148, v32, v33, v64 neg_lo:[1,0,0] neg_hi:[1,0,0]
	v_cvt_pk_f16_f32 v32, v34, v35
	v_and_b32_e32 v33, 0x7fff7fff, v32
	v_pk_fma_f16 v34, v33, s2, v164 op_sel_hi:[1,0,0]
	s_waitcnt vmcnt(0) lgkmcnt(9)
	v_mfma_f32_32x32x16_f16 v[16:31], v[88:91], v[80:83], 0
	v_pk_fma_f16 v34, v34, v33, s3 op_sel_hi:[1,1,0]
	v_and_b32_e32 v37, 0x7fff7fff, v36
	v_pk_mul_f16 v34, v33, v34
	v_pk_add_f16 v32, v33, v32
	v_exp_f16_e32 v35, v34
	v_exp_f16_sdwa v34, v34 dst_sel:DWORD dst_unused:UNUSED_PAD src0_sel:WORD_1
	v_pk_fma_f16 v64, v37, s2, v164 op_sel_hi:[1,0,0]
	v_mfma_f32_32x32x16_f16 v[16:31], v[178:181], v[116:119], v[16:31]
	v_pk_fma_f16 v64, v64, v37, s3 op_sel_hi:[1,1,0]
	v_pack_b32_f16 v34, v35, v34
	v_pk_fma_f16 v149, v33, v34, v32 neg_lo:[1,0,0] neg_hi:[1,0,0]
	ds_read_b128 v[32:35], v254 offset:35456
	v_pk_mul_f16 v64, v37, v64
	v_pk_add_f16 v36, v37, v36
	v_exp_f16_e32 v65, v64
	v_exp_f16_sdwa v64, v64 dst_sel:DWORD dst_unused:UNUSED_PAD src0_sel:WORD_1
	v_mfma_f32_32x32x16_f16 v[16:31], v[84:87], v[124:127], v[16:31]
	v_cvt_pk_f16_f32 v84, v38, v39
	v_and_b32_e32 v85, 0x7fff7fff, v84
	v_pack_b32_f16 v64, v65, v64
	v_pk_fma_f16 v150, v37, v64, v36 neg_lo:[1,0,0] neg_hi:[1,0,0]
	v_pk_fma_f16 v36, v85, s2, v164 op_sel_hi:[1,0,0]
	s_mov_b32 s6, 0x1b000
	v_pk_fma_f16 v64, v36, v85, s3 op_sel_hi:[1,1,0]
	ds_read_b128 v[36:39], v254 offset:39552
	s_waitcnt vmcnt(0) lgkmcnt(10)
	v_mfma_f32_32x32x16_f16 v[16:31], v[92:95], v[128:131], v[16:31]
	v_add_co_u32_e32 v204, vcc, s6, v156
	v_pk_mul_f16 v86, v85, v64
	s_nop 0
	v_addc_co_u32_e32 v205, vcc, 0, v157, vcc
	ds_read_b128 v[178:181], v255 offset:8192
	ds_read_b128 v[194:197], v254 offset:46720
	ds_read_b128 v[198:201], v254 offset:44672
	s_waitcnt vmcnt(0) lgkmcnt(9)
	v_mfma_f32_32x32x16_f16 v[16:31], v[72:75], v[132:135], v[16:31]
	v_cvt_pk_f16_f32 v40, v40, v41
	v_and_b32_e32 v41, 0x7fff7fff, v40
	v_pk_fma_f16 v88, v41, s2, v164 op_sel_hi:[1,0,0]
	v_exp_f16_e32 v87, v86
	v_pk_fma_f16 v88, v88, v41, s3 op_sel_hi:[1,1,0]
	v_exp_f16_sdwa v86, v86 dst_sel:DWORD dst_unused:UNUSED_PAD src0_sel:WORD_1
	v_pk_mul_f16 v88, v41, v88
	s_waitcnt vmcnt(0) lgkmcnt(8)
	v_mfma_f32_32x32x16_f16 v[64:79], v[76:79], v[80:83], 0
	v_exp_f16_e32 v89, v88
	v_exp_f16_sdwa v88, v88 dst_sel:DWORD dst_unused:UNUSED_PAD src0_sel:WORD_1
	v_pack_b32_f16 v86, v87, v86
	v_pk_add_f16 v84, v85, v84
	v_pk_add_f16 v40, v41, v40
	v_pk_fma_f16 v151, v85, v86, v84 neg_lo:[1,0,0] neg_hi:[1,0,0]
	v_pack_b32_f16 v84, v89, v88
	v_mfma_f32_32x32x16_f16 v[64:79], v[152:155], v[116:119], v[64:79]
	v_pk_fma_f16 v152, v41, v84, v40 neg_lo:[1,0,0] neg_hi:[1,0,0]
	v_cvt_pk_f16_f32 v153, v42, v43
	ds_read_b128 v[40:43], v254 offset:48768
	s_mov_b32 s6, 0x1a000
	v_add_co_u32_e32 v154, vcc, s6, v156
	s_mov_b32 s6, 0x19000
	v_mfma_f32_32x32x16_f16 v[64:79], v[170:173], v[124:127], v[64:79]
	v_addc_co_u32_e32 v155, vcc, 0, v157, vcc
	ds_read_b128 v[170:173], v254 offset:50816
	v_add_co_u32_e32 v162, vcc, s6, v156
	v_and_b32_e32 v159, 0x7fff7fff, v153
	s_nop 0
	v_addc_co_u32_e32 v163, vcc, 0, v157, vcc
	v_mfma_f32_32x32x16_f16 v[64:79], v[182:185], v[128:131], v[64:79]
	v_pk_fma_f16 v84, v159, s2, v164 op_sel_hi:[1,0,0]
	ds_read_b128 v[182:185], v255 offset:2048
	v_pk_fma_f16 v84, v84, v159, s3 op_sel_hi:[1,1,0]
	s_mov_b32 s6, 0x1c000
	v_pk_mul_f16 v84, v159, v84
	v_cvt_pk_f16_f32 v48, v48, v49
	v_exp_f16_e32 v165, v84
	s_waitcnt vmcnt(0) lgkmcnt(9)
	v_mfma_f32_32x32x16_f16 v[64:79], v[166:169], v[132:135], v[64:79]
	ds_read_b128 v[166:169], v255
	v_exp_f16_sdwa v206, v84 dst_sel:DWORD dst_unused:UNUSED_PAD src0_sel:WORD_1
	v_cvt_pk_f16_f32 v49, v50, v51
	v_cvt_pk_f16_f32 v50, v52, v53
	v_cvt_pk_f16_f32 v51, v54, v55
	v_cvt_pk_f16_f32 v24, v24, v25
	v_cvt_pk_f16_f32 v25, v26, v27
	v_mfma_f32_32x32x16_f16 v[80:95], v[190:193], v[80:83], 0
	v_cvt_pk_f16_f32 v26, v28, v29
	v_cvt_pk_f16_f32 v27, v30, v31
	ds_read_b128 v[28:31], v254 offset:49792
	v_cvt_pk_f16_f32 v20, v20, v21
	v_cvt_pk_f16_f32 v21, v22, v23
	v_pk_max_f16 v23, v21, 0
	v_pk_max_f16 v22, v20, 0
	s_waitcnt vmcnt(0) lgkmcnt(10)
	v_mfma_f32_32x32x16_f16 v[80:95], v[174:177], v[116:119], v[80:95]
	ds_read_b128 v[116:119], v255 offset:4096
	v_pk_max_f16 v176, v50, 0
	v_pk_max_f16 v175, v49, 0
	v_pk_max_f16 v174, v48, 0
	v_cvt_pk_f16_f32 v48, v56, v57
	v_cvt_pk_f16_f32 v49, v58, v59
	v_cvt_pk_f16_f32 v50, v60, v61
	v_mfma_f32_32x32x16_f16 v[80:95], v[186:189], v[124:127], v[80:95]
	v_add_co_u32_e32 v186, vcc, s6, v156
	v_pk_max_f16 v177, v51, 0
	s_nop 0
	v_addc_co_u32_e32 v187, vcc, 0, v157, vcc
	ds_read_b128 v[124:127], v255 offset:6144
	v_pk_max_f16 v27, v27, 0
	s_waitcnt vmcnt(0) lgkmcnt(11)
	v_mfma_f32_32x32x16_f16 v[80:95], v[32:35], v[128:131], v[80:95]
	v_cvt_pk_f16_f32 v32, v62, v63
	v_pk_max_f16 v131, v32, 0
	ds_read_b128 v[32:35], v255 offset:9216
	v_pk_max_f16 v130, v50, 0
	v_pk_max_f16 v129, v49, 0
	v_pk_max_f16 v128, v48, 0
	v_pk_max_f16 v26, v26, 0
	s_waitcnt vmcnt(0) lgkmcnt(11)
	v_mfma_f32_32x32x16_f16 v[80:95], v[36:39], v[132:135], v[80:95]
	v_cvt_pk_f16_f32 v36, v16, v17
	v_cvt_pk_f16_f32 v37, v18, v19
	ds_read_b128 v[16:19], v254 offset:45696
	ds_read_b128 v[132:135], v254 offset:47744
	v_cvt_pk_f16_f32 v38, v68, v69
	v_cvt_pk_f16_f32 v39, v70, v71
	ds_read_b128 v[68:71], v254 offset:51840
	s_waitcnt vmcnt(0) lgkmcnt(13)
	v_mfma_f32_32x32x16_f16 v[48:63], v[178:181], v[96:99], 0
	v_pk_max_f16 v21, v37, 0
	v_pk_max_f16 v20, v36, 0
	v_cvt_pk_f16_f32 v36, v64, v65
	v_cvt_pk_f16_f32 v37, v66, v67
	v_pk_max_f16 v65, v37, 0
	v_pk_max_f16 v64, v36, 0
	v_cvt_pk_f16_f32 v36, v72, v73
	s_waitcnt vmcnt(0) lgkmcnt(11)
	v_mfma_f32_32x32x16_f16 v[48:63], v[198:201], v[174:177], v[48:63]
	v_cvt_pk_f16_f32 v37, v74, v75
	ds_read_b128 v[72:75], v255 offset:1024
	v_pk_max_f16 v25, v25, 0
	v_pk_max_f16 v24, v24, 0
	v_pk_max_f16 v67, v39, 0
	v_pk_max_f16 v66, v38, 0
	ds_read_b128 v[160:163], v255 offset:3072
	v_mfma_f32_32x32x16_f16 v[48:63], v[194:197], v[128:131], v[48:63]
	v_cvt_pk_f16_f32 v38, v76, v77
	v_cvt_pk_f16_f32 v39, v78, v79
	v_pk_max_f16 v79, v39, 0
	v_pk_max_f16 v78, v38, 0
	v_pk_max_f16 v77, v37, 0
	v_pk_max_f16 v76, v36, 0
	v_cvt_pk_f16_f32 v36, v80, v81
	s_waitcnt vmcnt(0) lgkmcnt(12)
	v_mfma_f32_32x32x16_f16 v[48:63], v[40:43], v[20:23], v[48:63]
	v_cvt_pk_f16_f32 v38, v84, v85
	v_cvt_pk_f16_f32 v39, v86, v87
	ds_read_b128 v[84:87], v255 offset:5120
	v_cvt_pk_f16_f32 v37, v82, v83
	v_pk_max_f16 v80, v36, 0
	v_cvt_pk_f16_f32 v36, v92, v93
	s_mov_b32 s6, 0x20000
	s_waitcnt vmcnt(0) lgkmcnt(12)
	v_mfma_f32_32x32x16_f16 v[48:63], v[170:173], v[24:27], v[48:63]
	v_pk_max_f16 v83, v39, 0
	v_pk_max_f16 v81, v37, 0
	v_cvt_pk_f16_f32 v39, v90, v91
	v_cvt_pk_f16_f32 v37, v94, v95
	v_pk_max_f16 v90, v36, 0
	v_add_co_u32_e32 v36, vcc, s6, v156
	s_waitcnt vmcnt(0) lgkmcnt(10)
	v_mfma_f32_32x32x16_f16 v[48:63], v[166:169], v[64:67], v[48:63]
	v_pk_max_f16 v82, v38, 0
	v_pk_max_f16 v91, v37, 0
	v_addc_co_u32_e32 v37, vcc, 0, v157, vcc
	ds_read_b128 v[92:95], v255 offset:7168
	v_cvt_pk_f16_f32 v207, v44, v45
	v_and_b32_e32 v190, 0x7fff7fff, v207
	v_mfma_f32_32x32x16_f16 v[48:63], v[182:185], v[76:79], v[48:63]
	ds_read_b128 v[166:169], v255 offset:10240
	v_pk_fma_f16 v44, v190, s2, v164 op_sel_hi:[1,0,0]
	v_cvt_pk_f16_f32 v38, v88, v89
	v_pk_fma_f16 v44, v44, v190, s3 op_sel_hi:[1,1,0]
	v_pk_max_f16 v88, v38, 0
	v_pk_mul_f16 v44, v190, v44
	v_pk_add_f16 v38, v159, v153
	s_waitcnt vmcnt(0) lgkmcnt(10)
	v_mfma_f32_32x32x16_f16 v[48:63], v[116:119], v[80:83], v[48:63]
	ds_read_b128 v[116:119], v255 offset:26944
	v_exp_f16_e32 v45, v44
	v_exp_f16_sdwa v36, v44 dst_sel:DWORD dst_unused:UNUSED_PAD src0_sel:WORD_1
	v_pack_b32_f16 v37, v165, v206
	v_cvt_pk_f16_f32 v155, v46, v47
	v_pk_max_f16 v89, v39, 0
	v_pk_fma_f16 v153, v159, v37, v38 neg_lo:[1,0,0] neg_hi:[1,0,0]
	v_and_b32_e32 v159, 0x7fff7fff, v155
	s_waitcnt vmcnt(0) lgkmcnt(10)
	v_mfma_f32_32x32x16_f16 v[48:63], v[124:127], v[88:91], v[48:63]
	v_pk_fma_f16 v124, v159, s2, v164 op_sel_hi:[1,0,0]
	v_pack_b32_f16 v154, v45, v36
	v_pk_fma_f16 v124, v124, v159, s3 op_sel_hi:[1,1,0]
	v_pk_add_f16 v171, v190, v207
	v_pk_mul_f16 v165, v159, v124
	ds_read_b128 v[124:127], v255 offset:11264
	v_exp_f16_e32 v170, v165
	s_waitcnt vmcnt(0) lgkmcnt(10)
	v_mfma_f32_32x32x16_f16 v[32:47], v[32:35], v[96:99], 0
	v_exp_f16_sdwa v165, v165 dst_sel:DWORD dst_unused:UNUSED_PAD src0_sel:WORD_1
	v_pk_fma_f16 v154, v190, v154, v171 neg_lo:[1,0,0] neg_hi:[1,0,0]
	s_mov_b32 s6, 0x1e000
	v_cvt_pk_f16_f32 v4, v4, v5
	v_and_b32_e32 v5, 0x7fff7fff, v4
	v_cvt_pk_f16_f32 v56, v56, v57
	v_cvt_pk_f16_f32 v57, v58, v59
	s_waitcnt vmcnt(0) lgkmcnt(9)
	v_mfma_f32_32x32x16_f16 v[32:47], v[16:19], v[174:177], v[32:47]
	v_pack_b32_f16 v16, v170, v165
	ds_read_b128 v[170:173], v255 offset:12288
	v_add_co_u32_e32 v174, vcc, s6, v156
	v_cvt_pk_f16_f32 v18, v0, v1
	s_nop 0
	v_addc_co_u32_e32 v175, vcc, 0, v157, vcc
	s_waitcnt vmcnt(0) lgkmcnt(9)
	v_mfma_f32_32x32x16_f16 v[32:47], v[132:135], v[128:131], v[32:47]
	ds_read_b128 v[128:131], v255 offset:13312
	v_and_b32_e32 v19, 0x7fff7fff, v18
	ds_read_b128 v[132:135], v255 offset:14336
	v_pk_fma_f16 v0, v19, s2, v164 op_sel_hi:[1,0,0]
	v_pk_add_f16 v17, v159, v155
	v_pk_fma_f16 v0, v0, v19, s3 op_sel_hi:[1,1,0]
	s_mov_b32 s6, 0x1d000
	v_mfma_f32_32x32x16_f16 v[32:47], v[28:31], v[20:23], v[32:47]
	v_pk_mul_f16 v0, v19, v0
	v_pk_fma_f16 v155, v159, v16, v17 neg_lo:[1,0,0] neg_hi:[1,0,0]
	v_exp_f16_e32 v1, v0
	v_exp_f16_sdwa v0, v0 dst_sel:DWORD dst_unused:UNUSED_PAD src0_sel:WORD_1
	v_add_co_u32_e32 v16, vcc, s6, v156
	v_cvt_pk_f16_f32 v20, v2, v3
	s_nop 0
	v_addc_co_u32_e32 v17, vcc, 0, v157, vcc
	v_pack_b32_f16 v159, v1, v0
	s_waitcnt vmcnt(0) lgkmcnt(10)
	v_mfma_f32_32x32x16_f16 v[32:47], v[68:71], v[24:27], v[32:47]
	ds_read_b128 v[0:3], v255 offset:15360
	v_and_b32_e32 v21, 0x7fff7fff, v20
	v_pk_fma_f16 v22, v21, s2, v164 op_sel_hi:[1,0,0]
	v_pk_add_f16 v18, v19, v18
	v_pk_fma_f16 v22, v22, v21, s3 op_sel_hi:[1,1,0]
	v_pk_fma_f16 v68, v19, v159, v18 neg_lo:[1,0,0] neg_hi:[1,0,0]
	v_pk_mul_f16 v22, v21, v22
	s_waitcnt vmcnt(0) lgkmcnt(10)
	v_mfma_f32_32x32x16_f16 v[32:47], v[72:75], v[64:67], v[32:47]
	ds_read_b128 v[64:67], v255 offset:16384
	ds_read_b128 v[72:75], v255 offset:17728
	v_pk_fma_f16 v16, v5, s2, v164 op_sel_hi:[1,0,0]
	v_cvt_pk_f16_f32 v17, v50, v51
	v_pk_fma_f16 v70, v16, v5, s3 op_sel_hi:[1,1,0]
	v_cvt_pk_f16_f32 v16, v48, v49
	ds_read_b128 v[48:51], v255 offset:18752
	s_waitcnt vmcnt(0) lgkmcnt(12)
	v_mfma_f32_32x32x16_f16 v[32:47], v[160:163], v[76:79], v[32:47]
	v_exp_f16_e32 v23, v22
	v_exp_f16_sdwa v22, v22 dst_sel:DWORD dst_unused:UNUSED_PAD src0_sel:WORD_1
	ds_read_b128 v[76:79], v255 offset:19776
	v_pk_add_f16 v19, v21, v20
	v_cvt_pk_f16_f32 v58, v60, v61
	v_pack_b32_f16 v18, v23, v22
	v_pk_fma_f16 v69, v21, v18, v19 neg_lo:[1,0,0] neg_hi:[1,0,0]
	s_waitcnt vmcnt(0) lgkmcnt(12)
	v_mfma_f32_32x32x16_f16 v[32:47], v[84:87], v[80:83], v[32:47]
	v_cvt_pk_f16_f32 v18, v52, v53
	v_cvt_pk_f16_f32 v19, v54, v55
	v_pk_max_f16 v55, v19, 0
	v_pk_max_f16 v54, v18, 0
	v_pk_max_f16 v53, v17, 0
	v_pk_max_f16 v52, v16, 0
	v_cvt_pk_f16_f32 v59, v62, v63
	s_waitcnt vmcnt(0) lgkmcnt(9)
	v_mfma_f32_32x32x16_f16 v[16:31], v[116:119], v[96:99], 0
	ds_read_b128 v[60:63], v255 offset:20800
	v_pk_max_f16 v59, v59, 0
	v_pk_max_f16 v58, v58, 0
	v_pk_max_f16 v57, v57, 0
	v_pk_max_f16 v56, v56, 0
	v_cvt_pk_f16_f32 v6, v6, v7
	v_and_b32_e32 v7, 0x7fff7fff, v6
	v_mfma_f32_32x32x16_f16 v[32:47], v[92:95], v[88:91], v[32:47]
	v_pk_add_f16 v4, v5, v4
	s_mov_b32 s6, 0x1f000
	v_mfma_f32_32x32x16_f16 v[16:31], v[166:169], v[52:55], v[16:31]
	s_nop 8
	v_cvt_pk_f16_f32 v32, v32, v33
	v_cvt_pk_f16_f32 v33, v34, v35
	v_cvt_pk_f16_f32 v34, v36, v37
	v_cvt_pk_f16_f32 v35, v38, v39
	ds_read_b128 v[36:39], v255 offset:21824
	v_pk_max_f16 v35, v35, 0
	v_pk_max_f16 v34, v34, 0
	s_waitcnt vmcnt(0) lgkmcnt(10)
	v_mfma_f32_32x32x16_f16 v[16:31], v[124:127], v[56:59], v[16:31]
	v_pk_max_f16 v33, v33, 0
	v_pk_max_f16 v32, v32, 0
	v_cvt_pk_f16_f32 v40, v40, v41
	v_add_co_u32_e32 v56, vcc, s6, v156
	s_nop 1
	v_addc_co_u32_e32 v57, vcc, 0, v157, vcc
	s_waitcnt vmcnt(0) lgkmcnt(9)
	v_mfma_f32_32x32x16_f16 v[16:31], v[170:173], v[32:35], v[16:31]
	v_cvt_pk_f16_f32 v32, v42, v43
	v_cvt_pk_f16_f32 v33, v44, v45
	v_cvt_pk_f16_f32 v34, v46, v47
	v_pk_max_f16 v35, v34, 0
	v_pk_max_f16 v34, v33, 0
	v_pk_max_f16 v33, v32, 0
	v_pk_max_f16 v32, v40, 0
	ds_read_b128 v[52:55], v255 offset:22848
	s_waitcnt vmcnt(0) lgkmcnt(9)
	v_mfma_f32_32x32x16_f16 v[16:31], v[128:131], v[32:35], v[16:31]
	v_pk_fma_f16 v34, v7, s2, v164 op_sel_hi:[1,0,0]
	v_pk_mul_f16 v32, v5, v70
	v_pk_fma_f16 v34, v34, v7, s3 op_sel_hi:[1,1,0]
	v_exp_f16_e32 v33, v32
	v_exp_f16_sdwa v32, v32 dst_sel:DWORD dst_unused:UNUSED_PAD src0_sel:WORD_1
	v_pk_mul_f16 v34, v7, v34
	v_pack_b32_f16 v32, v33, v32
	s_waitcnt vmcnt(0) lgkmcnt(8)
	v_mfma_f32_32x32x16_f16 v[16:31], v[132:135], v[120:123], v[16:31]
	v_exp_f16_e32 v35, v34
	v_exp_f16_sdwa v34, v34 dst_sel:DWORD dst_unused:UNUSED_PAD src0_sel:WORD_1
	v_pk_fma_f16 v70, v5, v32, v4 neg_lo:[1,0,0] neg_hi:[1,0,0]
	v_pack_b32_f16 v4, v35, v34
	s_waitcnt vmcnt(0) lgkmcnt(7)
	v_mfma_f32_32x32x16_f16 v[16:31], v[0:3], v[136:139], v[16:31]
	v_pk_add_f16 v0, v7, v6
	s_nop 0
	v_pk_fma_f16 v71, v7, v4, v0 neg_lo:[1,0,0] neg_hi:[1,0,0]
	v_cvt_pk_f16_f32 v0, v8, v9
	v_and_b32_e32 v1, 0x7fff7fff, v0
	v_cvt_pk_f16_f32 v4, v10, v11
	v_pk_fma_f16 v2, v1, s2, v164 op_sel_hi:[1,0,0]
	s_waitcnt vmcnt(0) lgkmcnt(6)
	v_mfma_f32_32x32x16_f16 v[16:31], v[64:67], v[140:143], v[16:31]
	v_and_b32_e32 v5, 0x7fff7fff, v4
	v_pk_fma_f16 v2, v2, v1, s3 op_sel_hi:[1,1,0]
	v_pk_fma_f16 v6, v5, s2, v164 op_sel_hi:[1,0,0]
	v_pk_mul_f16 v2, v1, v2
	v_pk_fma_f16 v6, v6, v5, s3 op_sel_hi:[1,1,0]
	v_exp_f16_e32 v3, v2
	v_exp_f16_sdwa v2, v2 dst_sel:DWORD dst_unused:UNUSED_PAD src0_sel:WORD_1
	s_waitcnt vmcnt(0) lgkmcnt(5)
	v_mfma_f32_32x32x16_f16 v[16:31], v[72:75], v[144:147], v[16:31]
	v_pk_mul_f16 v6, v5, v6
	v_pk_add_f16 v0, v1, v0
	v_exp_f16_e32 v7, v6
	v_exp_f16_sdwa v6, v6 dst_sel:DWORD dst_unused:UNUSED_PAD src0_sel:WORD_1
	v_pack_b32_f16 v2, v3, v2
	v_pk_fma_f16 v0, v1, v2, v0 neg_lo:[1,0,0] neg_hi:[1,0,0]
	v_pk_add_f16 v2, v5, v4
	s_waitcnt vmcnt(0) lgkmcnt(4)
	v_mfma_f32_32x32x16_f16 v[16:31], v[48:51], v[148:151], v[16:31]
	v_pack_b32_f16 v1, v7, v6
	v_pk_fma_f16 v1, v5, v1, v2 neg_lo:[1,0,0] neg_hi:[1,0,0]
	v_cvt_pk_f16_f32 v2, v12, v13
	v_and_b32_e32 v3, 0x7fff7fff, v2
	v_cvt_pk_f16_f32 v6, v14, v15
	v_pk_fma_f16 v4, v3, s2, v164 op_sel_hi:[1,0,0]
	v_and_b32_e32 v7, 0x7fff7fff, v6
	s_waitcnt vmcnt(0) lgkmcnt(3)
	v_mfma_f32_32x32x16_f16 v[16:31], v[76:79], v[152:155], v[16:31]
	v_pk_fma_f16 v4, v4, v3, s3 op_sel_hi:[1,1,0]
	v_pk_fma_f16 v8, v7, s2, v164 op_sel_hi:[1,0,0]
	v_pk_mul_f16 v4, v3, v4
	v_pk_fma_f16 v8, v8, v7, s3 op_sel_hi:[1,1,0]
	v_exp_f16_e32 v5, v4
	v_exp_f16_sdwa v4, v4 dst_sel:DWORD dst_unused:UNUSED_PAD src0_sel:WORD_1
	v_pk_mul_f16 v8, v7, v8
	s_waitcnt vmcnt(0) lgkmcnt(2)
	v_mfma_f32_32x32x16_f16 v[16:31], v[60:63], v[68:71], v[16:31]
	v_exp_f16_e32 v9, v8
	v_exp_f16_sdwa v8, v8 dst_sel:DWORD dst_unused:UNUSED_PAD src0_sel:WORD_1
	v_pack_b32_f16 v4, v5, v4
	v_pk_add_f16 v2, v3, v2
	s_nop 0
	v_pk_fma_f16 v2, v3, v4, v2 neg_lo:[1,0,0] neg_hi:[1,0,0]
	v_pack_b32_f16 v3, v9, v8
	v_pk_add_f16 v4, v7, v6
	s_nop 0
	v_pk_fma_f16 v3, v7, v3, v4 neg_lo:[1,0,0] neg_hi:[1,0,0]
	ds_read_b128 v[4:7], v255 offset:24896
	s_waitcnt vmcnt(0) lgkmcnt(2)
	v_mfma_f32_32x32x16_f16 v[16:31], v[36:39], v[0:3], v[16:31]
	ds_read_b128 v[0:3], v255 offset:23872
	s_waitcnt vmcnt(0) lgkmcnt(2)
	v_mfma_f32_32x32x16_f16 v[16:31], v[52:55], v[104:107], v[16:31]
	s_waitcnt vmcnt(0) lgkmcnt(0)
	v_mfma_f32_32x32x16_f16 v[16:31], v[0:3], v[100:103], v[16:31]
	ds_read_b128 v[0:3], v255 offset:25920
	v_mfma_f32_32x32x16_f16 v[16:31], v[4:7], v[112:115], v[16:31]
	s_waitcnt vmcnt(0) lgkmcnt(0)
	v_mfma_f32_32x32x16_f16 v[16:31], v[0:3], v[108:111], v[16:31]
	s_nop 11
	ds_bpermute_b32 v3, v209, v16
	ds_bpermute_b32 v2, v209, v17
	ds_bpermute_b32 v1, v209, v18
	ds_bpermute_b32 v0, v209, v19
	s_and_saveexec_b64 s[2:3], s[0:1]
	s_cbranch_execz .LBB0_33
	v_max_f32_e32 v4, v17, v17
	v_max_f32_e32 v5, v16, v16
	v_max_f32_e32 v4, v5, v4
	v_max_f32_e32 v5, v19, v19
	v_max_f32_e32 v6, v18, v18
	v_max_f32_e32 v5, v6, v5
	s_waitcnt vmcnt(0) lgkmcnt(3)
	v_max3_f32 v6, v4, v5, v3
	v_sub_f32_e32 v4, v16, v6
	v_sub_f32_e32 v5, v17, v6
	v_sub_f32_e32 v7, v18, v6
	v_mul_f32_e32 v4, 0x3fb8aa3b, v4
	v_mul_f32_e32 v5, 0x3fb8aa3b, v5
	v_mul_f32_e32 v7, 0x3fb8aa3b, v7
	v_exp_f32_e32 v4, v4
	v_exp_f32_e32 v5, v5
	v_exp_f32_e32 v9, v7
	v_sub_f32_e32 v7, v19, v6
	v_mul_f32_e32 v7, 0x3fb8aa3b, v7
	v_sub_f32_e32 v6, v3, v6
	v_exp_f32_e32 v7, v7
	v_mul_f32_e32 v6, 0x3fb8aa3b, v6
	v_exp_f32_e32 v6, v6
	v_add_f32_e32 v8, v4, v5
	v_add_f32_e32 v8, v9, v8
	v_add_f32_e32 v8, v7, v8
	v_add_f32_e32 v8, v6, v8
	v_rcp_f32_e32 v8, v8
	s_waitcnt vmcnt(0) lgkmcnt(1)
	v_mul_f32_e32 v1, 0xbfb8aa3b, v1
	v_exp_f32_e32 v1, v1
	s_mov_b32 s1, 0x403fba14
	v_pk_mul_f32 v[6:7], v[6:7], v[8:9] op_sel_hi:[1,0]
	s_mov_b32 s0, 0x40f33a98
	v_pk_mul_f32 v[20:21], v[4:5], v[8:9] op_sel_hi:[1,0]
	v_pk_mul_f32 v[14:15], v[6:7], s[0:1]
	s_mov_b32 s0, 0x411e74af
	v_add_f32_e32 v4, v20, v21
	v_mul_f32_e32 v12, v9, v8
	v_fmac_f32_e32 v4, v9, v8
	v_pk_mul_f32 v[8:9], v[20:21], s[0:1]
	s_mov_b32 s3, 0x4108466c
	s_mov_b32 s2, s1
	v_add_f32_e32 v1, 1.0, v1
	v_mul_f32_e32 v13, 0x411e74af, v6
	v_pk_fma_f32 v[8:9], v[20:21], s[2:3], v[8:9] op_sel:[0,0,1] op_sel_hi:[1,1,0]
	s_mov_b32 s2, 0x40dd0c55
	s_mov_b32 s3, s0
	v_max_f32_e32 v2, v2, v2
	v_rcp_f32_e32 v1, v1
	v_mul_f32_e32 v7, 0x40c6de12, v7
	v_pk_fma_f32 v[8:9], v[12:13], s[2:3], v[8:9] op_sel_hi:[0,1,1]
	v_mov_b32_e32 v6, v15
	v_max_f32_e32 v2, 0xc1400000, v2
	v_pk_add_f32 v[6:7], v[6:7], v[8:9]
	v_mov_b32_e32 v15, v13
	v_min_f32_e32 v2, 0x41400000, v2
	v_pk_add_f32 v[6:7], v[14:15], v[6:7]
	s_mov_b32 s4, 0xbfb8aa3b
	v_mul_f32_e32 v4, v2, v4
	v_sub_f32_e32 v2, v7, v6
	v_fmac_f32_e32 v6, v1, v2
	s_waitcnt vmcnt(0) lgkmcnt(0)
	v_mul_f32_e64 v1, |v0|, s4
	v_exp_f32_e32 v1, v1
	v_max_f32_e32 v0, v0, v0
	v_mov_b32_e32 v2, 0x411e74af
	v_max_f32_e32 v0, 0, v0
	v_add_f32_e32 v1, 1.0, v1
	v_log_f32_e32 v1, v1
	v_med3_f32 v2, v6, s1, v2
	v_mul_f32_e32 v2, 0x3fb8aa3b, v2
	v_exp_f32_e32 v5, v2
	v_fmamk_f32 v0, v1, 0x3f317218, v0
	v_add_f32_e32 v0, 0x3dcccccd, v0
	v_max_f32_e32 v0, 0x3dcccccd, v0
	v_min_f32_e32 v6, 0x41200000, v0
	v_lshlrev_b32_e32 v0, 3, v158
	v_mov_b32_e32 v10, s38
	v_mov_b32_e32 v11, s39
	v_ashrrev_i32_e32 v1, 31, v0
	v_lshl_add_u64 v[8:9], v[0:1], 2, v[10:11]
	v_mov_b32_e32 v7, v16
	v_pk_mov_b32 v[0:1], v[16:17], v[18:19] op_sel:[1,0]
	v_mov_b32_e32 v2, v19
	global_store_dwordx4 v[8:9], v[4:7], off
	global_store_dwordx4 v[8:9], v[0:3], off offset:16
